# hoist buffer_inv sc1 (L1 invalidate) behind each seam's arrival atomic; arrival wait vmcnt(1)
# speedup vs baseline: 1.0065x; 1.0065x over previous
; __device__ __forceinline__ unsigned xb_ld(unsigned* p)              { return __hip_atomic_load(p, __ATOMIC_RELAXED, __HIP_MEMORY_SCOPE_AGENT); }
; __device__ __forceinline__ unsigned xb_add(unsigned* p, unsigned v) { return __hip_atomic_fetch_add(p, v, __ATOMIC_RELAXED, __HIP_MEMORY_SCOPE_AGENT); }
; #define XB_SPIN(cond, bar) do { unsigned _sp = 0; while (cond) { __builtin_amdgcn_s_sleep(1); \
;     if ((++_sp & 255u) == 0u) { if (xb_ld(&(bar)[XB_TMO])) break; if (_sp > XB_SPIN_CAP) { atomicAdd(&(bar)[XB_TMO], 1u); break; } } } } while (0)
; __device__ __forceinline__ void xcd_barrier(const XcdBarrier& b) {
;     ...
;     if (threadIdx.x == 0) {
;         unsigned* bar = b.bar;
;         __builtin_amdgcn_s_waitcnt(0);
;         unsigned nloc = b.st[0], nx = b.st[1];
;         if (nloc == 0u) { xcd_barrier_complete(bar, b.x, nloc, nx); b.st[0] = nloc; b.st[1] = nx; }
;         const unsigned old = xb_add(&bar[XB_XSUB(b.x)], 1u);
;         const unsigned gen = old / nloc;
;         if (old + 1u == (gen + 1u) * nloc) {
;             __builtin_amdgcn_fence(__ATOMIC_RELEASE, "agent");
;             asm volatile("s_waitcnt vmcnt(0)" ::: "memory");
;             const unsigned og = xb_add(&bar[XB_TOP], 1u);
;             const unsigned tg = og / nx;
;             if (og + 1u == (tg + 1u) * nx) xb_add(&bar[XB_TOPGEN], 1u);
;             else XB_SPIN(xb_ld(&bar[XB_TOPGEN]) == tg, bar);
;             __builtin_amdgcn_fence(__ATOMIC_ACQUIRE, "agent");
;             xb_add(&bar[XB_XGEN(b.x)], 1u);
;             asm volatile("s_waitcnt vmcnt(0)" ::: "memory");
;         } else {
;             XB_SPIN(xb_ld(&bar[XB_XGEN(b.x)]) == gen, bar);
.LBB0_88:
	s_mov_b64 s[6:7], exec
	s_lshl_b32 s3, s52, 8
	v_mbcnt_lo_u32_b32 v2, s6, 0
	s_add_u32 s4, s16, s3
	v_mbcnt_hi_u32_b32 v2, s7, v2
	s_addc_u32 s5, s17, 0
	v_cmp_eq_u32_e32 vcc, 0, v2
	s_and_saveexec_b64 s[8:9], vcc
	s_cbranch_execz .LBB0_90
	s_bcnt1_i32_b64 s3, s[6:7]
	v_mov_b32_e32 v4, 0x1000
	v_mov_b32_e32 v5, s3
	global_atomic_add v4, v4, v5, s[4:5] offset:1024 sc0
	buffer_inv sc1
.LBB0_90:
	s_or_b64 exec, exec, s[8:9]
	v_cvt_f32_u32_e32 v5, v3
	s_waitcnt vmcnt(1)
	v_readfirstlane_b32 s3, v4
	v_sub_u32_e32 v4, 0, v3
	v_rcp_iflag_f32_e32 v5, v5
	v_add_u32_e32 v6, s3, v2
	v_mul_f32_e32 v5, 0x4f7ffffe, v5
	v_cvt_u32_f32_e32 v5, v5
	v_mul_lo_u32 v2, v4, v5
	v_mul_hi_u32 v2, v5, v2
	v_add_u32_e32 v2, v5, v2
	v_mul_hi_u32 v2, v6, v2
	v_mul_lo_u32 v4, v2, v3
	v_sub_u32_e32 v4, v6, v4
	v_add_u32_e32 v5, 1, v2
	v_cmp_ge_u32_e32 vcc, v4, v3
	s_nop 1
	v_cndmask_b32_e32 v2, v2, v5, vcc
	v_sub_u32_e32 v5, v4, v3
	v_cndmask_b32_e32 v4, v4, v5, vcc
	v_add_u32_e32 v5, 1, v2
	v_cmp_ge_u32_e32 vcc, v4, v3
	v_add_u32_e32 v4, 1, v6
	s_nop 0
	v_cndmask_b32_e32 v2, v2, v5, vcc
	v_mul_lo_u32 v5, v3, v2
	v_add_u32_e32 v3, v5, v3
	v_cmp_ne_u32_e32 vcc, v4, v3
	s_and_saveexec_b64 s[6:7], vcc
	s_xor_b64 s[6:7], exec, s[6:7]
	s_cbranch_execz .LBB0_104
	s_waitcnt lgkmcnt(0)
	v_mov_b32_e32 v1, 0x2000
	global_load_dword v1, v1, s[4:5] offset:1024 sc1
	s_add_u32 s12, s4, 0x2400
	s_addc_u32 s13, s5, 0
	s_waitcnt vmcnt(0)
	v_cmp_eq_u32_e32 vcc, v1, v2
	s_and_saveexec_b64 s[8:9], vcc
	s_cbranch_execz .LBB0_103
	v_readlane_b32 s10, v252, 2
	v_readlane_b32 s11, v252, 3
	s_add_u32 s10, s10, 0x4200
	s_addc_u32 s11, s11, 0
	s_mov_b32 s3, 1
	s_mov_b64 s[14:15], 0
	v_mov_b32_e32 v1, 0
	s_branch .LBB0_94

; __device__ __forceinline__ unsigned xb_ld(unsigned* p)              { return __hip_atomic_load(p, __ATOMIC_RELAXED, __HIP_MEMORY_SCOPE_AGENT); }
; #define XB_SPIN(cond, bar) do { unsigned _sp = 0; while (cond) { __builtin_amdgcn_s_sleep(1); \
;     if ((++_sp & 255u) == 0u) { if (xb_ld(&(bar)[XB_TMO])) break; if (_sp > XB_SPIN_CAP) { atomicAdd(&(bar)[XB_TMO], 1u); break; } } } } while (0)
; __device__ __forceinline__ void xcd_barrier(const XcdBarrier& b) {
;     ...
;             XB_SPIN(xb_ld(&bar[XB_XGEN(b.x)]) == gen, bar);
;             __builtin_amdgcn_fence(__ATOMIC_ACQUIRE, "agent");
;             asm volatile("s_waitcnt vmcnt(0)" ::: "memory");
.LBB0_103:
	s_or_b64 exec, exec, s[8:9]
	s_waitcnt vmcnt(0)
	s_waitcnt vmcnt(0)

; __device__ __forceinline__ unsigned xb_ld(unsigned* p)              { return __hip_atomic_load(p, __ATOMIC_RELAXED, __HIP_MEMORY_SCOPE_AGENT); }
; __device__ __forceinline__ unsigned xb_add(unsigned* p, unsigned v) { return __hip_atomic_fetch_add(p, v, __ATOMIC_RELAXED, __HIP_MEMORY_SCOPE_AGENT); }
; #define XB_SPIN(cond, bar) do { unsigned _sp = 0; while (cond) { __builtin_amdgcn_s_sleep(1); \
;     if ((++_sp & 255u) == 0u) { if (xb_ld(&(bar)[XB_TMO])) break; if (_sp > XB_SPIN_CAP) { atomicAdd(&(bar)[XB_TMO], 1u); break; } } } } while (0)
; __device__ __forceinline__ void xcd_barrier(const XcdBarrier& b) {
;     ...
;             if (og + 1u == (tg + 1u) * nx) xb_add(&bar[XB_TOPGEN], 1u);
;             else XB_SPIN(xb_ld(&bar[XB_TOPGEN]) == tg, bar);
;             __builtin_amdgcn_fence(__ATOMIC_ACQUIRE, "agent");
;             xb_add(&bar[XB_XGEN(b.x)], 1u);
.LBB0_121:
	s_or_b64 exec, exec, s[6:7]
	s_mov_b64 s[6:7], exec
	v_mbcnt_lo_u32_b32 v1, s6, 0
	v_mbcnt_hi_u32_b32 v1, s7, v1
	v_cmp_eq_u32_e32 vcc, 0, v1
	s_waitcnt vmcnt(0)
	s_and_saveexec_b64 s[8:9], vcc
	s_cbranch_execz .LBB0_123
	s_bcnt1_i32_b64 s3, s[6:7]
	v_mov_b32_e32 v1, 0x2000
	v_mov_b32_e32 v2, s3
	global_atomic_add v1, v2, s[4:5] offset:1024

; __device__ __forceinline__ unsigned xb_ld(unsigned* p)              { return __hip_atomic_load(p, __ATOMIC_RELAXED, __HIP_MEMORY_SCOPE_AGENT); }
; __device__ __forceinline__ unsigned xb_add(unsigned* p, unsigned v) { return __hip_atomic_fetch_add(p, v, __ATOMIC_RELAXED, __HIP_MEMORY_SCOPE_AGENT); }
; #define XB_SPIN(cond, bar) do { unsigned _sp = 0; while (cond) { __builtin_amdgcn_s_sleep(1); \
;     if ((++_sp & 255u) == 0u) { if (xb_ld(&(bar)[XB_TMO])) break; if (_sp > XB_SPIN_CAP) { atomicAdd(&(bar)[XB_TMO], 1u); break; } } } } while (0)
; __device__ __forceinline__ void xcd_barrier(const XcdBarrier& b) {
;     ...
;     if (threadIdx.x == 0) {
;         unsigned* bar = b.bar;
;         __builtin_amdgcn_s_waitcnt(0);
;         unsigned nloc = b.st[0], nx = b.st[1];
;         if (nloc == 0u) { xcd_barrier_complete(bar, b.x, nloc, nx); b.st[0] = nloc; b.st[1] = nx; }
;         const unsigned old = xb_add(&bar[XB_XSUB(b.x)], 1u);
;         const unsigned gen = old / nloc;
;         if (old + 1u == (gen + 1u) * nloc) {
;             __builtin_amdgcn_fence(__ATOMIC_RELEASE, "agent");
;             asm volatile("s_waitcnt vmcnt(0)" ::: "memory");
;             const unsigned og = xb_add(&bar[XB_TOP], 1u);
;             const unsigned tg = og / nx;
;             if (og + 1u == (tg + 1u) * nx) xb_add(&bar[XB_TOPGEN], 1u);
;             else XB_SPIN(xb_ld(&bar[XB_TOPGEN]) == tg, bar);
;             __builtin_amdgcn_fence(__ATOMIC_ACQUIRE, "agent");
;             xb_add(&bar[XB_XGEN(b.x)], 1u);
;             asm volatile("s_waitcnt vmcnt(0)" ::: "memory");
;         } else {
;             XB_SPIN(xb_ld(&bar[XB_XGEN(b.x)]) == gen, bar);
.LBB0_152:
	s_mov_b64 s[4:5], exec
	s_lshl_b32 s2, s52, 8
	v_mbcnt_lo_u32_b32 v2, s4, 0
	s_add_u32 s2, s16, s2
	v_mbcnt_hi_u32_b32 v2, s5, v2
	s_addc_u32 s3, s17, 0
	v_cmp_eq_u32_e32 vcc, 0, v2
	s_and_saveexec_b64 s[6:7], vcc
	s_cbranch_execz .LBB0_154
	s_bcnt1_i32_b64 s4, s[4:5]
	v_mov_b32_e32 v4, 0x1000
	v_mov_b32_e32 v5, s4
	global_atomic_add v4, v4, v5, s[2:3] offset:1024 sc0
	buffer_inv sc1
.LBB0_154:
	s_or_b64 exec, exec, s[6:7]
	v_cvt_f32_u32_e32 v5, v3
	s_waitcnt vmcnt(1)
	v_readfirstlane_b32 s4, v4
	v_sub_u32_e32 v4, 0, v3
	v_rcp_iflag_f32_e32 v5, v5
	v_add_u32_e32 v6, s4, v2
	v_mul_f32_e32 v5, 0x4f7ffffe, v5
	v_cvt_u32_f32_e32 v5, v5
	v_mul_lo_u32 v2, v4, v5
	v_mul_hi_u32 v2, v5, v2
	v_add_u32_e32 v2, v5, v2
	v_mul_hi_u32 v2, v6, v2
	v_mul_lo_u32 v4, v2, v3
	v_sub_u32_e32 v4, v6, v4
	v_add_u32_e32 v5, 1, v2
	v_cmp_ge_u32_e32 vcc, v4, v3
	s_nop 1
	v_cndmask_b32_e32 v2, v2, v5, vcc
	v_sub_u32_e32 v5, v4, v3
	v_cndmask_b32_e32 v4, v4, v5, vcc
	v_add_u32_e32 v5, 1, v2
	v_cmp_ge_u32_e32 vcc, v4, v3
	v_add_u32_e32 v4, 1, v6
	s_nop 0
	v_cndmask_b32_e32 v2, v2, v5, vcc
	v_mul_lo_u32 v5, v3, v2
	v_add_u32_e32 v3, v5, v3
	v_cmp_ne_u32_e32 vcc, v4, v3
	s_and_saveexec_b64 s[4:5], vcc
	s_xor_b64 s[4:5], exec, s[4:5]
	s_cbranch_execz .LBB0_168
	s_waitcnt lgkmcnt(0)
	v_mov_b32_e32 v1, 0x2000
	global_load_dword v1, v1, s[2:3] offset:1024 sc1
	s_add_u32 s10, s2, 0x2400
	s_addc_u32 s11, s3, 0
	s_waitcnt vmcnt(0)
	v_cmp_eq_u32_e32 vcc, v1, v2
	s_and_saveexec_b64 s[6:7], vcc
	s_cbranch_execz .LBB0_167
	v_readlane_b32 s8, v252, 2
	v_readlane_b32 s9, v252, 3
	s_add_u32 s8, s8, 0x4200
	s_addc_u32 s9, s9, 0
	s_mov_b32 s24, 1
	s_mov_b64 s[12:13], 0
	v_mov_b32_e32 v1, 0
	s_branch .LBB0_158

; __device__ __forceinline__ unsigned xb_ld(unsigned* p)              { return __hip_atomic_load(p, __ATOMIC_RELAXED, __HIP_MEMORY_SCOPE_AGENT); }
; #define XB_SPIN(cond, bar) do { unsigned _sp = 0; while (cond) { __builtin_amdgcn_s_sleep(1); \
;     if ((++_sp & 255u) == 0u) { if (xb_ld(&(bar)[XB_TMO])) break; if (_sp > XB_SPIN_CAP) { atomicAdd(&(bar)[XB_TMO], 1u); break; } } } } while (0)
; __device__ __forceinline__ void xcd_barrier(const XcdBarrier& b) {
;     ...
;             XB_SPIN(xb_ld(&bar[XB_XGEN(b.x)]) == gen, bar);
;             __builtin_amdgcn_fence(__ATOMIC_ACQUIRE, "agent");
;             asm volatile("s_waitcnt vmcnt(0)" ::: "memory");
.LBB0_167:
	s_or_b64 exec, exec, s[6:7]
	s_waitcnt vmcnt(0)
	s_waitcnt vmcnt(0)

; __device__ __forceinline__ unsigned xb_ld(unsigned* p)              { return __hip_atomic_load(p, __ATOMIC_RELAXED, __HIP_MEMORY_SCOPE_AGENT); }
; __device__ __forceinline__ unsigned xb_add(unsigned* p, unsigned v) { return __hip_atomic_fetch_add(p, v, __ATOMIC_RELAXED, __HIP_MEMORY_SCOPE_AGENT); }
; #define XB_SPIN(cond, bar) do { unsigned _sp = 0; while (cond) { __builtin_amdgcn_s_sleep(1); \
;     if ((++_sp & 255u) == 0u) { if (xb_ld(&(bar)[XB_TMO])) break; if (_sp > XB_SPIN_CAP) { atomicAdd(&(bar)[XB_TMO], 1u); break; } } } } while (0)
; __device__ __forceinline__ void xcd_barrier(const XcdBarrier& b) {
;     ...
;             if (og + 1u == (tg + 1u) * nx) xb_add(&bar[XB_TOPGEN], 1u);
;             else XB_SPIN(xb_ld(&bar[XB_TOPGEN]) == tg, bar);
;             __builtin_amdgcn_fence(__ATOMIC_ACQUIRE, "agent");
;             xb_add(&bar[XB_XGEN(b.x)], 1u);
.LBB0_185:
	s_or_b64 exec, exec, s[4:5]
	s_mov_b64 s[4:5], exec
	v_mbcnt_lo_u32_b32 v1, s4, 0
	v_mbcnt_hi_u32_b32 v1, s5, v1
	v_cmp_eq_u32_e32 vcc, 0, v1
	s_waitcnt vmcnt(0)
	s_and_saveexec_b64 s[6:7], vcc
	s_cbranch_execz .LBB0_187
	s_bcnt1_i32_b64 s4, s[4:5]
	v_mov_b32_e32 v1, 0x2000
	v_mov_b32_e32 v2, s4
	global_atomic_add v1, v2, s[2:3] offset:1024

; __device__ __forceinline__ unsigned xb_ld(unsigned* p)              { return __hip_atomic_load(p, __ATOMIC_RELAXED, __HIP_MEMORY_SCOPE_AGENT); }
; __device__ __forceinline__ unsigned xb_add(unsigned* p, unsigned v) { return __hip_atomic_fetch_add(p, v, __ATOMIC_RELAXED, __HIP_MEMORY_SCOPE_AGENT); }
; #define XB_SPIN(cond, bar) do { unsigned _sp = 0; while (cond) { __builtin_amdgcn_s_sleep(1); \
;     if ((++_sp & 255u) == 0u) { if (xb_ld(&(bar)[XB_TMO])) break; if (_sp > XB_SPIN_CAP) { atomicAdd(&(bar)[XB_TMO], 1u); break; } } } } while (0)
; __device__ __forceinline__ void xcd_local_barrier(const XcdBarrier& b, const bool wave0) {
;     asm volatile("s_waitcnt vmcnt(0)" ::: "memory");
;     __syncthreads();
;     if (wave0 && __builtin_amdgcn_mbcnt_hi(~0u, __builtin_amdgcn_mbcnt_lo(~0u, 0u)) == 0u) {
;         unsigned* bar = b.bar;
;         __builtin_amdgcn_s_waitcnt(0);
;         const unsigned nloc = b.st[0];
;         const unsigned old = xb_add(&bar[XB_LSUB(b.x)], 1u);
;         const unsigned gen = old / nloc;
;         if (old + 1u == (gen + 1u) * nloc) xb_add(&bar[XB_LGEN(b.x)], 1u);
;         else XB_SPIN(xb_ld(&bar[XB_LGEN(b.x)]) == gen, bar);
.LBB0_220:
	v_readlane_b32 s0, v254, 56
	s_or_b32 s5, s0, 3
	s_cmp_lt_i32 s5, s93
	v_readlane_b32 s2, v254, 61
	s_cselect_b64 s[0:1], -1, 0
	v_readlane_b32 s3, v254, 62
	s_and_b64 s[2:3], s[2:3], s[0:1]
	s_andn2_b64 vcc, exec, s[2:3]
	s_cbranch_vccnz .LBB0_298
	v_readlane_b32 s2, v252, 8
	v_readlane_b32 s3, v252, 9
	s_andn2_b64 vcc, exec, s[2:3]
	s_cbranch_vccnz .LBB0_236
	s_waitcnt vmcnt(0)
	s_cmp_lg_u32 s51, 0
	s_waitcnt vmcnt(0)
	s_barrier
	s_cbranch_scc1 .LBB0_243
	v_cmp_eq_u32_e32 vcc, 0, v225
	s_and_saveexec_b64 s[2:3], vcc
	s_cbranch_execz .LBB0_242
	v_readlane_b32 s6, v254, 36
	s_waitcnt vmcnt(0) expcnt(0) lgkmcnt(0)
	s_mov_b64 s[38:39], exec
	v_mov_b32_e32 v1, s6
	ds_read_b32 v2, v1
	v_mbcnt_lo_u32_b32 v1, s38, 0
	v_mbcnt_hi_u32_b32 v1, s39, v1
	v_cmp_eq_u32_e32 vcc, 0, v1
	s_and_saveexec_b64 s[40:41], vcc
	s_cbranch_execz .LBB0_226
	s_bcnt1_i32_b64 s6, s[38:39]
	v_mov_b32_e32 v4, s6
	v_readlane_b32 s6, v252, 14
	v_readlane_b32 s7, v252, 15
	s_nop 4
	global_atomic_add v4, v3, v4, s[6:7] sc0
	buffer_inv sc1
.LBB0_226:
	s_or_b64 exec, exec, s[40:41]
	s_waitcnt vmcnt(1)
	v_readfirstlane_b32 s6, v4
	s_waitcnt lgkmcnt(0)
	v_sub_u32_e32 v5, 0, v2
	s_mov_b64 s[40:41], -1
	v_add_u32_e32 v4, s6, v1
	v_cvt_f32_u32_e32 v1, v2
	v_readlane_b32 s6, v252, 16
	v_readlane_b32 s7, v252, 17
	v_rcp_iflag_f32_e32 v1, v1
	s_nop 0
	v_mul_f32_e32 v1, 0x4f7ffffe, v1
	v_cvt_u32_f32_e32 v1, v1
	v_mul_lo_u32 v5, v5, v1
	v_mul_hi_u32 v5, v1, v5
	v_add_u32_e32 v1, v1, v5
	v_mul_hi_u32 v1, v4, v1
	v_mul_lo_u32 v5, v1, v2
	v_sub_u32_e32 v5, v4, v5
	v_cmp_ge_u32_e32 vcc, v5, v2
	v_add_u32_e32 v6, 1, v1
	v_add_u32_e32 v4, 1, v4
	v_cndmask_b32_e32 v1, v1, v6, vcc
	v_sub_u32_e32 v6, v5, v2
	v_cndmask_b32_e32 v5, v5, v6, vcc
	v_cmp_ge_u32_e32 vcc, v5, v2
	v_add_u32_e32 v5, 1, v1
	s_nop 0
	v_cndmask_b32_e32 v1, v1, v5, vcc
	v_mul_lo_u32 v5, v2, v1
	v_add_u32_e32 v2, v5, v2
	v_cmp_ne_u32_e32 vcc, v4, v2
	v_mov_b64_e32 v[4:5], s[6:7]
	s_and_saveexec_b64 s[38:39], vcc
	s_cbranch_execz .LBB0_239
	v_readlane_b32 s6, v252, 16
	v_readlane_b32 s7, v252, 17
	s_mov_b64 s[42:43], 0
	s_nop 3
	global_load_dword v2, v3, s[6:7] sc1
	s_waitcnt vmcnt(0)
	v_cmp_eq_u32_e32 vcc, v2, v1
	s_and_saveexec_b64 s[40:41], vcc
	s_cbranch_execz .LBB0_238
	s_mov_b32 s22, s51
	s_mov_b32 s6, 1
	s_branch .LBB0_230

; __device__ __forceinline__ unsigned xb_ld(unsigned* p)              { return __hip_atomic_load(p, __ATOMIC_RELAXED, __HIP_MEMORY_SCOPE_AGENT); }
; #define XB_SPIN(cond, bar) do { unsigned _sp = 0; while (cond) { __builtin_amdgcn_s_sleep(1); \
;     if ((++_sp & 255u) == 0u) { if (xb_ld(&(bar)[XB_TMO])) break; if (_sp > XB_SPIN_CAP) { atomicAdd(&(bar)[XB_TMO], 1u); break; } } } } while (0)
; __device__ __forceinline__ void xcd_local_barrier(const XcdBarrier& b, const bool wave0) {
;     ...
;         else XB_SPIN(xb_ld(&bar[XB_LGEN(b.x)]) == gen, bar);
;         __builtin_amdgcn_fence(__ATOMIC_ACQUIRE, "agent");
;         asm volatile("s_waitcnt vmcnt(0)" ::: "memory");
.LBB0_241:
	s_or_b64 exec, exec, s[38:39]
	s_waitcnt vmcnt(0)
	s_waitcnt vmcnt(0)

; __device__ __forceinline__ unsigned xb_ld(unsigned* p)              { return __hip_atomic_load(p, __ATOMIC_RELAXED, __HIP_MEMORY_SCOPE_AGENT); }
; __device__ __forceinline__ unsigned xb_add(unsigned* p, unsigned v) { return __hip_atomic_fetch_add(p, v, __ATOMIC_RELAXED, __HIP_MEMORY_SCOPE_AGENT); }
; #define XB_SPIN(cond, bar) do { unsigned _sp = 0; while (cond) { __builtin_amdgcn_s_sleep(1); \
;     if ((++_sp & 255u) == 0u) { if (xb_ld(&(bar)[XB_TMO])) break; if (_sp > XB_SPIN_CAP) { atomicAdd(&(bar)[XB_TMO], 1u); break; } } } } while (0)
; __device__ __forceinline__ void xcd_barrier(const XcdBarrier& b) {
;     ...
;         const unsigned old = xb_add(&bar[XB_XSUB(b.x)], 1u);
;         const unsigned gen = old / nloc;
;         if (old + 1u == (gen + 1u) * nloc) {
;             __builtin_amdgcn_fence(__ATOMIC_RELEASE, "agent");
;             asm volatile("s_waitcnt vmcnt(0)" ::: "memory");
;             const unsigned og = xb_add(&bar[XB_TOP], 1u);
;             const unsigned tg = og / nx;
;             if (og + 1u == (tg + 1u) * nx) xb_add(&bar[XB_TOPGEN], 1u);
;             else XB_SPIN(xb_ld(&bar[XB_TOPGEN]) == tg, bar);
;             __builtin_amdgcn_fence(__ATOMIC_ACQUIRE, "agent");
;             xb_add(&bar[XB_XGEN(b.x)], 1u);
;             asm volatile("s_waitcnt vmcnt(0)" ::: "memory");
;         } else {
;             XB_SPIN(xb_ld(&bar[XB_XGEN(b.x)]) == gen, bar);
.LBB0_260:
	s_mov_b64 s[40:41], exec
	v_mbcnt_lo_u32_b32 v1, s40, 0
	v_mbcnt_hi_u32_b32 v1, s41, v1
	v_cmp_eq_u32_e32 vcc, 0, v1
	s_and_saveexec_b64 s[38:39], vcc
	s_cbranch_execz .LBB0_262
	s_bcnt1_i32_b64 s6, s[40:41]
	v_mov_b32_e32 v5, s6
	v_readlane_b32 s6, v253, 20
	v_readlane_b32 s7, v253, 21
	s_nop 4
	global_atomic_add v5, v3, v5, s[6:7] sc0
	buffer_inv sc1
.LBB0_262:
	s_or_b64 exec, exec, s[38:39]
	v_cvt_f32_u32_e32 v6, v4
	s_waitcnt vmcnt(1)
	v_readfirstlane_b32 s6, v5
	v_sub_u32_e32 v5, 0, v4
	v_rcp_iflag_f32_e32 v6, v6
	v_add_u32_e32 v7, s6, v1
	v_mul_f32_e32 v6, 0x4f7ffffe, v6
	v_cvt_u32_f32_e32 v6, v6
	v_mul_lo_u32 v1, v5, v6
	v_mul_hi_u32 v1, v6, v1
	v_add_u32_e32 v1, v6, v1
	v_mul_hi_u32 v1, v7, v1
	v_mul_lo_u32 v5, v1, v4
	v_sub_u32_e32 v5, v7, v5
	v_add_u32_e32 v6, 1, v1
	v_cmp_ge_u32_e32 vcc, v5, v4
	s_nop 1
	v_cndmask_b32_e32 v1, v1, v6, vcc
	v_sub_u32_e32 v6, v5, v4
	v_cndmask_b32_e32 v5, v5, v6, vcc
	v_add_u32_e32 v6, 1, v1
	v_cmp_ge_u32_e32 vcc, v5, v4
	v_add_u32_e32 v5, 1, v7
	s_nop 0
	v_cndmask_b32_e32 v1, v1, v6, vcc
	v_mul_lo_u32 v6, v4, v1
	v_add_u32_e32 v4, v6, v4
	v_cmp_ne_u32_e32 vcc, v5, v4
	s_and_saveexec_b64 s[6:7], vcc
	s_xor_b64 s[38:39], exec, s[6:7]
	s_cbranch_execz .LBB0_276
	v_readlane_b32 s6, v253, 22
	v_readlane_b32 s7, v253, 23
	s_waitcnt lgkmcnt(0)
	s_nop 3
	global_load_dword v2, v3, s[6:7] sc1
	s_waitcnt vmcnt(0)
	v_cmp_eq_u32_e32 vcc, v2, v1
	s_and_saveexec_b64 s[40:41], vcc
	s_cbranch_execz .LBB0_275
	s_mov_b32 s22, s51
	s_mov_b32 s6, 1
	s_mov_b64 s[42:43], 0
	s_branch .LBB0_266

; __device__ __forceinline__ unsigned xb_ld(unsigned* p)              { return __hip_atomic_load(p, __ATOMIC_RELAXED, __HIP_MEMORY_SCOPE_AGENT); }
; #define XB_SPIN(cond, bar) do { unsigned _sp = 0; while (cond) { __builtin_amdgcn_s_sleep(1); \
;     if ((++_sp & 255u) == 0u) { if (xb_ld(&(bar)[XB_TMO])) break; if (_sp > XB_SPIN_CAP) { atomicAdd(&(bar)[XB_TMO], 1u); break; } } } } while (0)
; __device__ __forceinline__ void xcd_barrier(const XcdBarrier& b) {
;     ...
;             XB_SPIN(xb_ld(&bar[XB_XGEN(b.x)]) == gen, bar);
;             __builtin_amdgcn_fence(__ATOMIC_ACQUIRE, "agent");
;             asm volatile("s_waitcnt vmcnt(0)" ::: "memory");
.LBB0_275:
	s_or_b64 exec, exec, s[40:41]
	s_waitcnt vmcnt(0)
	s_waitcnt vmcnt(0)

; __device__ __forceinline__ unsigned xb_ld(unsigned* p)              { return __hip_atomic_load(p, __ATOMIC_RELAXED, __HIP_MEMORY_SCOPE_AGENT); }
; __device__ __forceinline__ unsigned xb_add(unsigned* p, unsigned v) { return __hip_atomic_fetch_add(p, v, __ATOMIC_RELAXED, __HIP_MEMORY_SCOPE_AGENT); }
; #define XB_SPIN(cond, bar) do { unsigned _sp = 0; while (cond) { __builtin_amdgcn_s_sleep(1); \
;     if ((++_sp & 255u) == 0u) { if (xb_ld(&(bar)[XB_TMO])) break; if (_sp > XB_SPIN_CAP) { atomicAdd(&(bar)[XB_TMO], 1u); break; } } } } while (0)
; __device__ __forceinline__ void xcd_barrier(const XcdBarrier& b) {
;     ...
;             if (og + 1u == (tg + 1u) * nx) xb_add(&bar[XB_TOPGEN], 1u);
;             else XB_SPIN(xb_ld(&bar[XB_TOPGEN]) == tg, bar);
;             __builtin_amdgcn_fence(__ATOMIC_ACQUIRE, "agent");
;             xb_add(&bar[XB_XGEN(b.x)], 1u);
.LBB0_293:
	s_or_b64 exec, exec, s[38:39]
	s_mov_b64 s[38:39], exec
	v_mbcnt_lo_u32_b32 v1, s38, 0
	v_mbcnt_hi_u32_b32 v1, s39, v1
	v_cmp_eq_u32_e32 vcc, 0, v1
	s_waitcnt vmcnt(0)
	s_and_saveexec_b64 s[40:41], vcc
	s_cbranch_execz .LBB0_295
	s_bcnt1_i32_b64 s6, s[38:39]
	v_mov_b32_e32 v1, s6
	v_readlane_b32 s6, v253, 22
	v_readlane_b32 s7, v253, 23
	s_nop 4
	global_atomic_add v3, v1, s[6:7]

; __device__ __forceinline__ unsigned xb_add(unsigned* p, unsigned v) { return __hip_atomic_fetch_add(p, v, __ATOMIC_RELAXED, __HIP_MEMORY_SCOPE_AGENT); }
; __device__ __forceinline__ void xcd_local_barrier(const XcdBarrier& b, const bool wave0) {
;     asm volatile("s_waitcnt vmcnt(0)" ::: "memory");
;     __syncthreads();
;     if (wave0 && __builtin_amdgcn_mbcnt_hi(~0u, __builtin_amdgcn_mbcnt_lo(~0u, 0u)) == 0u) {
;         unsigned* bar = b.bar;
;         __builtin_amdgcn_s_waitcnt(0);
;         const unsigned nloc = b.st[0];
;         const unsigned old = xb_add(&bar[XB_LSUB(b.x)], 1u);
.LBB0_566:
	v_readlane_b32 s0, v254, 56
	s_or_b32 s5, s0, 5
	s_cmp_lt_i32 s5, s93
	v_readlane_b32 s2, v255, 5
	s_cselect_b64 s[0:1], -1, 0
	v_readlane_b32 s3, v255, 6
	s_and_b64 s[2:3], s[2:3], s[0:1]
	s_andn2_b64 vcc, exec, s[2:3]
	s_cbranch_vccnz .LBB0_644
	v_readlane_b32 s2, v252, 8
	v_readlane_b32 s3, v252, 9
	s_andn2_b64 vcc, exec, s[2:3]
	s_cbranch_vccnz .LBB0_582
	s_waitcnt vmcnt(0)
	s_cmp_lg_u32 s51, 0
	s_waitcnt vmcnt(0)
	s_barrier
	s_cbranch_scc1 .LBB0_589
	v_cmp_eq_u32_e32 vcc, 0, v225
	s_and_saveexec_b64 s[2:3], vcc
	s_cbranch_execz .LBB0_588
	v_readlane_b32 s6, v254, 36
	s_waitcnt vmcnt(0) expcnt(0) lgkmcnt(0)
	s_mov_b64 s[38:39], exec
	v_mov_b32_e32 v1, s6
	ds_read_b32 v2, v1
	v_mbcnt_lo_u32_b32 v1, s38, 0
	v_mbcnt_hi_u32_b32 v1, s39, v1
	v_cmp_eq_u32_e32 vcc, 0, v1
	s_and_saveexec_b64 s[40:41], vcc
	s_cbranch_execz .LBB0_572
	s_bcnt1_i32_b64 s6, s[38:39]
	v_mov_b32_e32 v4, s6
	v_readlane_b32 s6, v252, 14
	v_readlane_b32 s7, v252, 15
	s_nop 4
	global_atomic_add v4, v3, v4, s[6:7] sc0
	buffer_inv sc1

; __device__ __forceinline__ unsigned xb_add(unsigned* p, unsigned v) { return __hip_atomic_fetch_add(p, v, __ATOMIC_RELAXED, __HIP_MEMORY_SCOPE_AGENT); }
; __device__ __forceinline__ void xcd_local_barrier(const XcdBarrier& b, const bool wave0) {
;     asm volatile("s_waitcnt vmcnt(0)" ::: "memory");
;     __syncthreads();
;     if (wave0 && __builtin_amdgcn_mbcnt_hi(~0u, __builtin_amdgcn_mbcnt_lo(~0u, 0u)) == 0u) {
;         unsigned* bar = b.bar;
;         __builtin_amdgcn_s_waitcnt(0);
;         const unsigned nloc = b.st[0];
;         const unsigned old = xb_add(&bar[XB_LSUB(b.x)], 1u);
.LBB0_674:
	v_readlane_b32 s2, v254, 56
	s_or_b32 s5, s2, 6
	s_cmp_lt_i32 s5, s93
	s_cselect_b64 s[2:3], -1, 0
	s_and_b64 s[0:1], s[0:1], s[2:3]
	s_mov_b64 s[2:3], 0
	s_andn2_b64 vcc, exec, s[0:1]
	s_mov_b64 s[0:1], 0
	s_cbranch_vccnz .LBB0_752
	v_readlane_b32 s0, v252, 8
	v_readlane_b32 s1, v252, 9
	s_andn2_b64 vcc, exec, s[0:1]
	s_cbranch_vccnz .LBB0_690
	s_waitcnt vmcnt(0)
	s_cmp_lg_u32 s51, 0
	s_waitcnt vmcnt(0)
	s_barrier
	s_cbranch_scc1 .LBB0_697
	v_cmp_eq_u32_e32 vcc, 0, v225
	s_and_saveexec_b64 s[0:1], vcc
	s_cbranch_execz .LBB0_696
	v_readlane_b32 s6, v254, 36
	s_waitcnt vmcnt(0) expcnt(0) lgkmcnt(0)
	s_mov_b64 s[38:39], exec
	v_mov_b32_e32 v1, s6
	ds_read_b32 v2, v1
	v_mbcnt_lo_u32_b32 v1, s38, 0
	v_mbcnt_hi_u32_b32 v1, s39, v1
	v_cmp_eq_u32_e32 vcc, 0, v1
	s_and_saveexec_b64 s[40:41], vcc
	s_cbranch_execz .LBB0_680
	s_bcnt1_i32_b64 s6, s[38:39]
	v_mov_b32_e32 v4, s6
	v_readlane_b32 s6, v252, 14
	v_readlane_b32 s7, v252, 15
	s_nop 4
	global_atomic_add v4, v3, v4, s[6:7] sc0
	buffer_inv sc1

; __device__ __forceinline__ unsigned xb_ld(unsigned* p)              { return __hip_atomic_load(p, __ATOMIC_RELAXED, __HIP_MEMORY_SCOPE_AGENT); }
; __device__ __forceinline__ unsigned xb_add(unsigned* p, unsigned v) { return __hip_atomic_fetch_add(p, v, __ATOMIC_RELAXED, __HIP_MEMORY_SCOPE_AGENT); }
; #define XB_SPIN(cond, bar) do { unsigned _sp = 0; while (cond) { __builtin_amdgcn_s_sleep(1); \
;     if ((++_sp & 255u) == 0u) { if (xb_ld(&(bar)[XB_TMO])) break; if (_sp > XB_SPIN_CAP) { atomicAdd(&(bar)[XB_TMO], 1u); break; } } } } while (0)
; __device__ __forceinline__ void xcd_local_barrier(const XcdBarrier& b, const bool wave0) {
;     asm volatile("s_waitcnt vmcnt(0)" ::: "memory");
;     __syncthreads();
;     if (wave0 && __builtin_amdgcn_mbcnt_hi(~0u, __builtin_amdgcn_mbcnt_lo(~0u, 0u)) == 0u) {
;         unsigned* bar = b.bar;
;         __builtin_amdgcn_s_waitcnt(0);
;         const unsigned nloc = b.st[0];
;         const unsigned old = xb_add(&bar[XB_LSUB(b.x)], 1u);
;         const unsigned gen = old / nloc;
;         if (old + 1u == (gen + 1u) * nloc) xb_add(&bar[XB_LGEN(b.x)], 1u);
;         else XB_SPIN(xb_ld(&bar[XB_LGEN(b.x)]) == gen, bar);
.LBB0_781:
	v_readlane_b32 s2, v254, 56
	s_or_b32 s2, s2, 3
	s_cmp_lt_i32 s2, s93
	v_readlane_b32 s6, v254, 61
	s_cselect_b64 s[2:3], -1, 0
	v_readlane_b32 s7, v254, 62
	s_and_b64 s[2:3], s[6:7], s[2:3]
	s_andn2_b64 vcc, exec, s[2:3]
	s_cbranch_vccnz .LBB0_859
	v_readlane_b32 s2, v252, 8
	v_readlane_b32 s3, v252, 9
	s_andn2_b64 vcc, exec, s[2:3]
	s_cbranch_vccnz .LBB0_797
	s_waitcnt vmcnt(0)
	s_cmp_lg_u32 s90, 0
	s_waitcnt vmcnt(0)
	s_barrier
	s_cbranch_scc1 .LBB0_804
	v_cmp_eq_u32_e32 vcc, 0, v225
	s_and_saveexec_b64 s[2:3], vcc
	s_cbranch_execz .LBB0_803
	v_readlane_b32 s5, v254, 36
	s_waitcnt vmcnt(0) expcnt(0) lgkmcnt(0)
	s_mov_b64 s[40:41], exec
	v_mov_b32_e32 v1, s5
	ds_read_b32 v2, v1
	v_mbcnt_lo_u32_b32 v1, s40, 0
	v_mbcnt_hi_u32_b32 v1, s41, v1
	v_cmp_eq_u32_e32 vcc, 0, v1
	s_and_saveexec_b64 s[42:43], vcc
	s_cbranch_execz .LBB0_787
	s_bcnt1_i32_b64 s5, s[40:41]
	v_readlane_b32 s6, v252, 14
	v_mov_b32_e32 v4, s5
	v_readlane_b32 s7, v252, 15
	s_nop 4
	global_atomic_add v4, v3, v4, s[6:7] sc0
	buffer_inv sc1
.LBB0_787:
	s_or_b64 exec, exec, s[42:43]
	s_waitcnt vmcnt(1)
	v_readfirstlane_b32 s5, v4
	s_waitcnt lgkmcnt(0)
	v_sub_u32_e32 v5, 0, v2
	v_readlane_b32 s6, v252, 16
	v_add_u32_e32 v4, s5, v1
	v_cvt_f32_u32_e32 v1, v2
	v_readlane_b32 s7, v252, 17
	s_mov_b64 s[42:43], -1
	v_rcp_iflag_f32_e32 v1, v1
	s_nop 0
	v_mul_f32_e32 v1, 0x4f7ffffe, v1
	v_cvt_u32_f32_e32 v1, v1
	v_mul_lo_u32 v5, v5, v1
	v_mul_hi_u32 v5, v1, v5
	v_add_u32_e32 v1, v1, v5
	v_mul_hi_u32 v1, v4, v1
	v_mul_lo_u32 v5, v1, v2
	v_sub_u32_e32 v5, v4, v5
	v_cmp_ge_u32_e32 vcc, v5, v2
	v_add_u32_e32 v6, 1, v1
	v_add_u32_e32 v4, 1, v4
	v_cndmask_b32_e32 v1, v1, v6, vcc
	v_sub_u32_e32 v6, v5, v2
	v_cndmask_b32_e32 v5, v5, v6, vcc
	v_cmp_ge_u32_e32 vcc, v5, v2
	v_add_u32_e32 v5, 1, v1
	s_nop 0
	v_cndmask_b32_e32 v1, v1, v5, vcc
	v_mul_lo_u32 v5, v2, v1
	v_add_u32_e32 v2, v5, v2
	v_cmp_ne_u32_e32 vcc, v4, v2
	v_mov_b64_e32 v[4:5], s[6:7]
	s_and_saveexec_b64 s[40:41], vcc
	s_cbranch_execz .LBB0_800
	v_readlane_b32 s6, v252, 16
	v_readlane_b32 s7, v252, 17
	s_mov_b64 s[44:45], 0
	s_nop 3
	global_load_dword v2, v3, s[6:7] sc1
	s_waitcnt vmcnt(0)
	v_cmp_eq_u32_e32 vcc, v2, v1
	s_and_saveexec_b64 s[42:43], vcc
	s_cbranch_execz .LBB0_799
	s_mov_b32 s5, 1
	s_branch .LBB0_791

; __device__ __forceinline__ unsigned xb_ld(unsigned* p)              { return __hip_atomic_load(p, __ATOMIC_RELAXED, __HIP_MEMORY_SCOPE_AGENT); }
; __device__ __forceinline__ unsigned xb_add(unsigned* p, unsigned v) { return __hip_atomic_fetch_add(p, v, __ATOMIC_RELAXED, __HIP_MEMORY_SCOPE_AGENT); }
; #define XB_SPIN(cond, bar) do { unsigned _sp = 0; while (cond) { __builtin_amdgcn_s_sleep(1); \
;     if ((++_sp & 255u) == 0u) { if (xb_ld(&(bar)[XB_TMO])) break; if (_sp > XB_SPIN_CAP) { atomicAdd(&(bar)[XB_TMO], 1u); break; } } } } while (0)
; __device__ __forceinline__ void xcd_barrier(const XcdBarrier& b) {
;     ...
;         const unsigned old = xb_add(&bar[XB_XSUB(b.x)], 1u);
;         const unsigned gen = old / nloc;
;         if (old + 1u == (gen + 1u) * nloc) {
;             __builtin_amdgcn_fence(__ATOMIC_RELEASE, "agent");
;             asm volatile("s_waitcnt vmcnt(0)" ::: "memory");
;             const unsigned og = xb_add(&bar[XB_TOP], 1u);
;             const unsigned tg = og / nx;
;             if (og + 1u == (tg + 1u) * nx) xb_add(&bar[XB_TOPGEN], 1u);
;             else XB_SPIN(xb_ld(&bar[XB_TOPGEN]) == tg, bar);
;             __builtin_amdgcn_fence(__ATOMIC_ACQUIRE, "agent");
;             xb_add(&bar[XB_XGEN(b.x)], 1u);
;             asm volatile("s_waitcnt vmcnt(0)" ::: "memory");
;         } else {
;             XB_SPIN(xb_ld(&bar[XB_XGEN(b.x)]) == gen, bar);
.LBB0_821:
	s_mov_b64 s[42:43], exec
	v_mbcnt_lo_u32_b32 v1, s42, 0
	v_mbcnt_hi_u32_b32 v1, s43, v1
	v_cmp_eq_u32_e32 vcc, 0, v1
	s_and_saveexec_b64 s[40:41], vcc
	s_cbranch_execz .LBB0_823
	s_bcnt1_i32_b64 s5, s[42:43]
	v_readlane_b32 s6, v253, 20
	v_mov_b32_e32 v5, s5
	v_readlane_b32 s7, v253, 21
	s_nop 4
	global_atomic_add v5, v3, v5, s[6:7] sc0
	buffer_inv sc1
.LBB0_823:
	s_or_b64 exec, exec, s[40:41]
	v_cvt_f32_u32_e32 v6, v4
	s_waitcnt vmcnt(1)
	v_readfirstlane_b32 s5, v5
	v_sub_u32_e32 v5, 0, v4
	v_rcp_iflag_f32_e32 v6, v6
	v_add_u32_e32 v7, s5, v1
	v_mul_f32_e32 v6, 0x4f7ffffe, v6
	v_cvt_u32_f32_e32 v6, v6
	v_mul_lo_u32 v1, v5, v6
	v_mul_hi_u32 v1, v6, v1
	v_add_u32_e32 v1, v6, v1
	v_mul_hi_u32 v1, v7, v1
	v_mul_lo_u32 v5, v1, v4
	v_sub_u32_e32 v5, v7, v5
	v_add_u32_e32 v6, 1, v1
	v_cmp_ge_u32_e32 vcc, v5, v4
	s_nop 1
	v_cndmask_b32_e32 v1, v1, v6, vcc
	v_sub_u32_e32 v6, v5, v4
	v_cndmask_b32_e32 v5, v5, v6, vcc
	v_add_u32_e32 v6, 1, v1
	v_cmp_ge_u32_e32 vcc, v5, v4
	v_add_u32_e32 v5, 1, v7
	s_nop 0
	v_cndmask_b32_e32 v1, v1, v6, vcc
	v_mul_lo_u32 v6, v4, v1
	v_add_u32_e32 v4, v6, v4
	v_cmp_ne_u32_e32 vcc, v5, v4
	s_and_saveexec_b64 s[6:7], vcc
	s_xor_b64 s[40:41], exec, s[6:7]
	s_cbranch_execz .LBB0_837
	v_readlane_b32 s6, v253, 22
	v_readlane_b32 s7, v253, 23
	s_waitcnt lgkmcnt(0)
	s_nop 3
	global_load_dword v2, v3, s[6:7] sc1
	s_waitcnt vmcnt(0)
	v_cmp_eq_u32_e32 vcc, v2, v1
	s_and_saveexec_b64 s[42:43], vcc
	s_cbranch_execz .LBB0_836
	s_mov_b32 s5, 1
	s_mov_b64 s[44:45], 0
	s_branch .LBB0_827

; __device__ __forceinline__ unsigned xb_ld(unsigned* p)              { return __hip_atomic_load(p, __ATOMIC_RELAXED, __HIP_MEMORY_SCOPE_AGENT); }
; #define XB_SPIN(cond, bar) do { unsigned _sp = 0; while (cond) { __builtin_amdgcn_s_sleep(1); \
;     if ((++_sp & 255u) == 0u) { if (xb_ld(&(bar)[XB_TMO])) break; if (_sp > XB_SPIN_CAP) { atomicAdd(&(bar)[XB_TMO], 1u); break; } } } } while (0)
; __device__ __forceinline__ void xcd_barrier(const XcdBarrier& b) {
;     ...
;             XB_SPIN(xb_ld(&bar[XB_XGEN(b.x)]) == gen, bar);
;             __builtin_amdgcn_fence(__ATOMIC_ACQUIRE, "agent");
;             asm volatile("s_waitcnt vmcnt(0)" ::: "memory");
.LBB0_836:
	s_or_b64 exec, exec, s[42:43]
	s_waitcnt vmcnt(0)
	s_waitcnt vmcnt(0)

; __device__ __forceinline__ unsigned xb_ld(unsigned* p)              { return __hip_atomic_load(p, __ATOMIC_RELAXED, __HIP_MEMORY_SCOPE_AGENT); }
; __device__ __forceinline__ unsigned xb_add(unsigned* p, unsigned v) { return __hip_atomic_fetch_add(p, v, __ATOMIC_RELAXED, __HIP_MEMORY_SCOPE_AGENT); }
; #define XB_SPIN(cond, bar) do { unsigned _sp = 0; while (cond) { __builtin_amdgcn_s_sleep(1); \
;     if ((++_sp & 255u) == 0u) { if (xb_ld(&(bar)[XB_TMO])) break; if (_sp > XB_SPIN_CAP) { atomicAdd(&(bar)[XB_TMO], 1u); break; } } } } while (0)
; __device__ __forceinline__ void xcd_barrier(const XcdBarrier& b) {
;     ...
;             if (og + 1u == (tg + 1u) * nx) xb_add(&bar[XB_TOPGEN], 1u);
;             else XB_SPIN(xb_ld(&bar[XB_TOPGEN]) == tg, bar);
;             __builtin_amdgcn_fence(__ATOMIC_ACQUIRE, "agent");
;             xb_add(&bar[XB_XGEN(b.x)], 1u);
.LBB0_854:
	s_or_b64 exec, exec, s[40:41]
	s_mov_b64 s[40:41], exec
	v_mbcnt_lo_u32_b32 v1, s40, 0
	v_mbcnt_hi_u32_b32 v1, s41, v1
	v_cmp_eq_u32_e32 vcc, 0, v1
	s_waitcnt vmcnt(0)
	s_and_saveexec_b64 s[42:43], vcc
	s_cbranch_execz .LBB0_856
	s_bcnt1_i32_b64 s5, s[40:41]
	v_readlane_b32 s6, v253, 22
	v_mov_b32_e32 v1, s5
	v_readlane_b32 s7, v253, 23
	s_nop 4
	global_atomic_add v3, v1, s[6:7]

; __device__ __forceinline__ unsigned xb_ld(unsigned* p)              { return __hip_atomic_load(p, __ATOMIC_RELAXED, __HIP_MEMORY_SCOPE_AGENT); }
; __device__ __forceinline__ unsigned xb_add(unsigned* p, unsigned v) { return __hip_atomic_fetch_add(p, v, __ATOMIC_RELAXED, __HIP_MEMORY_SCOPE_AGENT); }
; #define XB_SPIN(cond, bar) do { unsigned _sp = 0; while (cond) { __builtin_amdgcn_s_sleep(1); \
;     if ((++_sp & 255u) == 0u) { if (xb_ld(&(bar)[XB_TMO])) break; if (_sp > XB_SPIN_CAP) { atomicAdd(&(bar)[XB_TMO], 1u); break; } } } } while (0)
; __device__ __forceinline__ void xcd_local_barrier(const XcdBarrier& b, const bool wave0) {
;     asm volatile("s_waitcnt vmcnt(0)" ::: "memory");
;     __syncthreads();
;     if (wave0 && __builtin_amdgcn_mbcnt_hi(~0u, __builtin_amdgcn_mbcnt_lo(~0u, 0u)) == 0u) {
;         unsigned* bar = b.bar;
;         __builtin_amdgcn_s_waitcnt(0);
;         const unsigned nloc = b.st[0];
;         const unsigned old = xb_add(&bar[XB_LSUB(b.x)], 1u);
;         const unsigned gen = old / nloc;
;         if (old + 1u == (gen + 1u) * nloc) xb_add(&bar[XB_LGEN(b.x)], 1u);
;         else XB_SPIN(xb_ld(&bar[XB_LGEN(b.x)]) == gen, bar);
.LBB0_1070:
	v_readlane_b32 s5, v254, 56
	s_or_b32 s5, s5, 5
	s_cmp_lt_i32 s5, s93
	s_cselect_b64 s[40:41], -1, 0
	s_and_b64 s[2:3], s[2:3], s[40:41]
	s_andn2_b64 vcc, exec, s[2:3]
	s_cbranch_vccnz .LBB0_1148
	v_readlane_b32 s2, v252, 8
	v_readlane_b32 s3, v252, 9
	s_andn2_b64 vcc, exec, s[2:3]
	s_cbranch_vccnz .LBB0_1086
	s_waitcnt vmcnt(0)
	s_cmp_lg_u32 s90, 0
	s_waitcnt vmcnt(0)
	s_barrier
	s_cbranch_scc1 .LBB0_1093
	v_cmp_eq_u32_e32 vcc, 0, v225
	s_and_saveexec_b64 s[2:3], vcc
	s_cbranch_execz .LBB0_1092
	v_readlane_b32 s6, v254, 36
	s_waitcnt vmcnt(0) expcnt(0) lgkmcnt(0)
	s_mov_b64 s[42:43], exec
	v_mov_b32_e32 v1, s6
	ds_read_b32 v2, v1
	v_mbcnt_lo_u32_b32 v1, s42, 0
	v_mbcnt_hi_u32_b32 v1, s43, v1
	v_cmp_eq_u32_e32 vcc, 0, v1
	s_and_saveexec_b64 s[44:45], vcc
	s_cbranch_execz .LBB0_1076
	s_bcnt1_i32_b64 s6, s[42:43]
	v_mov_b32_e32 v4, s6
	v_readlane_b32 s6, v252, 14
	v_readlane_b32 s7, v252, 15
	s_nop 4
	global_atomic_add v4, v3, v4, s[6:7] sc0
	buffer_inv sc1
.LBB0_1076:
	s_or_b64 exec, exec, s[44:45]
	s_waitcnt vmcnt(1)
	v_readfirstlane_b32 s6, v4
	s_waitcnt lgkmcnt(0)
	v_sub_u32_e32 v5, 0, v2
	s_mov_b64 s[44:45], -1
	v_add_u32_e32 v4, s6, v1
	v_cvt_f32_u32_e32 v1, v2
	v_readlane_b32 s6, v252, 16
	v_readlane_b32 s7, v252, 17
	v_rcp_iflag_f32_e32 v1, v1
	s_nop 0
	v_mul_f32_e32 v1, 0x4f7ffffe, v1
	v_cvt_u32_f32_e32 v1, v1
	v_mul_lo_u32 v5, v5, v1
	v_mul_hi_u32 v5, v1, v5
	v_add_u32_e32 v1, v1, v5
	v_mul_hi_u32 v1, v4, v1
	v_mul_lo_u32 v5, v1, v2
	v_sub_u32_e32 v5, v4, v5
	v_cmp_ge_u32_e32 vcc, v5, v2
	v_add_u32_e32 v6, 1, v1
	v_add_u32_e32 v4, 1, v4
	v_cndmask_b32_e32 v1, v1, v6, vcc
	v_sub_u32_e32 v6, v5, v2
	v_cndmask_b32_e32 v5, v5, v6, vcc
	v_cmp_ge_u32_e32 vcc, v5, v2
	v_add_u32_e32 v5, 1, v1
	s_nop 0
	v_cndmask_b32_e32 v1, v1, v5, vcc
	v_mul_lo_u32 v5, v2, v1
	v_add_u32_e32 v2, v5, v2
	v_cmp_ne_u32_e32 vcc, v4, v2
	v_mov_b64_e32 v[4:5], s[6:7]
	s_and_saveexec_b64 s[42:43], vcc
	s_cbranch_execz .LBB0_1089
	v_readlane_b32 s6, v252, 16
	v_readlane_b32 s7, v252, 17
	s_mov_b64 s[46:47], 0
	s_nop 3
	global_load_dword v2, v3, s[6:7] sc1
	s_waitcnt vmcnt(0)
	v_cmp_eq_u32_e32 vcc, v2, v1
	s_and_saveexec_b64 s[44:45], vcc
	s_cbranch_execz .LBB0_1088
	s_mov_b32 s6, 1
	s_branch .LBB0_1080

; __device__ __forceinline__ unsigned xb_ld(unsigned* p)              { return __hip_atomic_load(p, __ATOMIC_RELAXED, __HIP_MEMORY_SCOPE_AGENT); }
; __device__ __forceinline__ unsigned xb_add(unsigned* p, unsigned v) { return __hip_atomic_fetch_add(p, v, __ATOMIC_RELAXED, __HIP_MEMORY_SCOPE_AGENT); }
; #define XB_SPIN(cond, bar) do { unsigned _sp = 0; while (cond) { __builtin_amdgcn_s_sleep(1); \
;     if ((++_sp & 255u) == 0u) { if (xb_ld(&(bar)[XB_TMO])) break; if (_sp > XB_SPIN_CAP) { atomicAdd(&(bar)[XB_TMO], 1u); break; } } } } while (0)
; __device__ __forceinline__ void xcd_barrier(const XcdBarrier& b) {
;     ...
;         const unsigned old = xb_add(&bar[XB_XSUB(b.x)], 1u);
;         const unsigned gen = old / nloc;
;         if (old + 1u == (gen + 1u) * nloc) {
;             __builtin_amdgcn_fence(__ATOMIC_RELEASE, "agent");
;             asm volatile("s_waitcnt vmcnt(0)" ::: "memory");
;             const unsigned og = xb_add(&bar[XB_TOP], 1u);
;             const unsigned tg = og / nx;
;             if (og + 1u == (tg + 1u) * nx) xb_add(&bar[XB_TOPGEN], 1u);
;             else XB_SPIN(xb_ld(&bar[XB_TOPGEN]) == tg, bar);
;             __builtin_amdgcn_fence(__ATOMIC_ACQUIRE, "agent");
;             xb_add(&bar[XB_XGEN(b.x)], 1u);
;             asm volatile("s_waitcnt vmcnt(0)" ::: "memory");
;         } else {
;             XB_SPIN(xb_ld(&bar[XB_XGEN(b.x)]) == gen, bar);
.LBB0_1110:
	s_mov_b64 s[44:45], exec
	v_mbcnt_lo_u32_b32 v1, s44, 0
	v_mbcnt_hi_u32_b32 v1, s45, v1
	v_cmp_eq_u32_e32 vcc, 0, v1
	s_and_saveexec_b64 s[42:43], vcc
	s_cbranch_execz .LBB0_1112
	s_bcnt1_i32_b64 s6, s[44:45]
	v_mov_b32_e32 v5, s6
	v_readlane_b32 s6, v253, 20
	v_readlane_b32 s7, v253, 21
	s_nop 4
	global_atomic_add v5, v3, v5, s[6:7] sc0
	buffer_inv sc1
.LBB0_1112:
	s_or_b64 exec, exec, s[42:43]
	v_cvt_f32_u32_e32 v6, v4
	s_waitcnt vmcnt(1)
	v_readfirstlane_b32 s6, v5
	v_sub_u32_e32 v5, 0, v4
	v_rcp_iflag_f32_e32 v6, v6
	v_add_u32_e32 v7, s6, v1
	v_mul_f32_e32 v6, 0x4f7ffffe, v6
	v_cvt_u32_f32_e32 v6, v6
	v_mul_lo_u32 v1, v5, v6
	v_mul_hi_u32 v1, v6, v1
	v_add_u32_e32 v1, v6, v1
	v_mul_hi_u32 v1, v7, v1
	v_mul_lo_u32 v5, v1, v4
	v_sub_u32_e32 v5, v7, v5
	v_add_u32_e32 v6, 1, v1
	v_cmp_ge_u32_e32 vcc, v5, v4
	s_nop 1
	v_cndmask_b32_e32 v1, v1, v6, vcc
	v_sub_u32_e32 v6, v5, v4
	v_cndmask_b32_e32 v5, v5, v6, vcc
	v_add_u32_e32 v6, 1, v1
	v_cmp_ge_u32_e32 vcc, v5, v4
	v_add_u32_e32 v5, 1, v7
	s_nop 0
	v_cndmask_b32_e32 v1, v1, v6, vcc
	v_mul_lo_u32 v6, v4, v1
	v_add_u32_e32 v4, v6, v4
	v_cmp_ne_u32_e32 vcc, v5, v4
	s_and_saveexec_b64 s[6:7], vcc
	s_xor_b64 s[42:43], exec, s[6:7]
	s_cbranch_execz .LBB0_1126
	v_readlane_b32 s6, v253, 22
	v_readlane_b32 s7, v253, 23
	s_waitcnt lgkmcnt(0)
	s_nop 3
	global_load_dword v2, v3, s[6:7] sc1
	s_waitcnt vmcnt(0)
	v_cmp_eq_u32_e32 vcc, v2, v1
	s_and_saveexec_b64 s[44:45], vcc
	s_cbranch_execz .LBB0_1125
	s_mov_b32 s6, 1
	s_mov_b64 s[46:47], 0
	s_branch .LBB0_1116

; __device__ __forceinline__ unsigned xb_ld(unsigned* p)              { return __hip_atomic_load(p, __ATOMIC_RELAXED, __HIP_MEMORY_SCOPE_AGENT); }
; #define XB_SPIN(cond, bar) do { unsigned _sp = 0; while (cond) { __builtin_amdgcn_s_sleep(1); \
;     if ((++_sp & 255u) == 0u) { if (xb_ld(&(bar)[XB_TMO])) break; if (_sp > XB_SPIN_CAP) { atomicAdd(&(bar)[XB_TMO], 1u); break; } } } } while (0)
; __device__ __forceinline__ void xcd_barrier(const XcdBarrier& b) {
;     ...
;             XB_SPIN(xb_ld(&bar[XB_XGEN(b.x)]) == gen, bar);
;             __builtin_amdgcn_fence(__ATOMIC_ACQUIRE, "agent");
;             asm volatile("s_waitcnt vmcnt(0)" ::: "memory");
.LBB0_1125:
	s_or_b64 exec, exec, s[44:45]
	s_waitcnt vmcnt(0)
	s_waitcnt vmcnt(0)

; __device__ __forceinline__ unsigned xb_ld(unsigned* p)              { return __hip_atomic_load(p, __ATOMIC_RELAXED, __HIP_MEMORY_SCOPE_AGENT); }
; __device__ __forceinline__ unsigned xb_add(unsigned* p, unsigned v) { return __hip_atomic_fetch_add(p, v, __ATOMIC_RELAXED, __HIP_MEMORY_SCOPE_AGENT); }
; #define XB_SPIN(cond, bar) do { unsigned _sp = 0; while (cond) { __builtin_amdgcn_s_sleep(1); \
;     if ((++_sp & 255u) == 0u) { if (xb_ld(&(bar)[XB_TMO])) break; if (_sp > XB_SPIN_CAP) { atomicAdd(&(bar)[XB_TMO], 1u); break; } } } } while (0)
; __device__ __forceinline__ void xcd_barrier(const XcdBarrier& b) {
;     ...
;             if (og + 1u == (tg + 1u) * nx) xb_add(&bar[XB_TOPGEN], 1u);
;             else XB_SPIN(xb_ld(&bar[XB_TOPGEN]) == tg, bar);
;             __builtin_amdgcn_fence(__ATOMIC_ACQUIRE, "agent");
;             xb_add(&bar[XB_XGEN(b.x)], 1u);
.LBB0_1143:
	s_or_b64 exec, exec, s[42:43]
	s_mov_b64 s[42:43], exec
	v_mbcnt_lo_u32_b32 v1, s42, 0
	v_mbcnt_hi_u32_b32 v1, s43, v1
	v_cmp_eq_u32_e32 vcc, 0, v1
	s_waitcnt vmcnt(0)
	s_and_saveexec_b64 s[44:45], vcc
	s_cbranch_execz .LBB0_1145
	s_bcnt1_i32_b64 s6, s[42:43]
	v_mov_b32_e32 v1, s6
	v_readlane_b32 s6, v253, 22
	v_readlane_b32 s7, v253, 23
	s_nop 4
	global_atomic_add v3, v1, s[6:7]

; __device__ __forceinline__ unsigned xb_ld(unsigned* p)              { return __hip_atomic_load(p, __ATOMIC_RELAXED, __HIP_MEMORY_SCOPE_AGENT); }
; __device__ __forceinline__ unsigned xb_add(unsigned* p, unsigned v) { return __hip_atomic_fetch_add(p, v, __ATOMIC_RELAXED, __HIP_MEMORY_SCOPE_AGENT); }
; #define XB_SPIN(cond, bar) do { unsigned _sp = 0; while (cond) { __builtin_amdgcn_s_sleep(1); \
;     if ((++_sp & 255u) == 0u) { if (xb_ld(&(bar)[XB_TMO])) break; if (_sp > XB_SPIN_CAP) { atomicAdd(&(bar)[XB_TMO], 1u); break; } } } } while (0)
; __device__ __forceinline__ void xcd_local_barrier(const XcdBarrier& b, const bool wave0) {
;     asm volatile("s_waitcnt vmcnt(0)" ::: "memory");
;     __syncthreads();
;     if (wave0 && __builtin_amdgcn_mbcnt_hi(~0u, __builtin_amdgcn_mbcnt_lo(~0u, 0u)) == 0u) {
;         unsigned* bar = b.bar;
;         __builtin_amdgcn_s_waitcnt(0);
;         const unsigned nloc = b.st[0];
;         const unsigned old = xb_add(&bar[XB_LSUB(b.x)], 1u);
;         const unsigned gen = old / nloc;
;         if (old + 1u == (gen + 1u) * nloc) xb_add(&bar[XB_LGEN(b.x)], 1u);
;         else XB_SPIN(xb_ld(&bar[XB_LGEN(b.x)]) == gen, bar);
.LBB0_1177:
	v_readlane_b32 s5, v254, 56
	s_or_b32 s5, s5, 6
	s_cmp_lt_i32 s5, s93
	s_cselect_b64 s[6:7], -1, 0
	s_and_b64 s[2:3], s[2:3], s[6:7]
	s_andn2_b64 vcc, exec, s[2:3]
	s_cbranch_vccnz .LBB0_1255
	v_readlane_b32 s0, v252, 8
	v_readlane_b32 s1, v252, 9
	s_andn2_b64 vcc, exec, s[0:1]
	s_cbranch_vccnz .LBB0_1193
	s_waitcnt vmcnt(0)
	s_cmp_lg_u32 s51, 0
	s_waitcnt vmcnt(0)
	s_barrier
	s_cbranch_scc1 .LBB0_1200
	v_cmp_eq_u32_e32 vcc, 0, v225
	s_and_saveexec_b64 s[0:1], vcc
	s_cbranch_execz .LBB0_1199
	v_readlane_b32 s6, v254, 36
	s_waitcnt vmcnt(0) expcnt(0) lgkmcnt(0)
	s_mov_b64 s[2:3], exec
	v_mov_b32_e32 v0, s6
	ds_read_b32 v0, v0
	v_mbcnt_lo_u32_b32 v1, s2, 0
	v_mbcnt_hi_u32_b32 v1, s3, v1
	v_cmp_eq_u32_e32 vcc, 0, v1
	s_and_saveexec_b64 s[38:39], vcc
	s_cbranch_execz .LBB0_1183
	s_bcnt1_i32_b64 s2, s[2:3]
	v_mov_b32_e32 v2, s2
	v_readlane_b32 s2, v252, 14
	v_readlane_b32 s3, v252, 15
	s_nop 4
	global_atomic_add v2, v3, v2, s[2:3] sc0
	buffer_inv sc1
.LBB0_1183:
	s_or_b64 exec, exec, s[38:39]
	s_waitcnt vmcnt(1)
	v_readfirstlane_b32 s2, v2
	s_waitcnt lgkmcnt(0)
	v_cvt_f32_u32_e32 v2, v0
	v_sub_u32_e32 v4, 0, v0
	v_add_u32_e32 v1, s2, v1
	v_readlane_b32 s2, v252, 16
	v_rcp_iflag_f32_e32 v2, v2
	v_readlane_b32 s3, v252, 17
	s_mov_b64 s[38:39], -1
	v_mul_f32_e32 v2, 0x4f7ffffe, v2
	v_cvt_u32_f32_e32 v2, v2
	v_mul_lo_u32 v4, v4, v2
	v_mul_hi_u32 v4, v2, v4
	v_add_u32_e32 v2, v2, v4
	v_mul_hi_u32 v2, v1, v2
	v_mul_lo_u32 v4, v2, v0
	v_sub_u32_e32 v4, v1, v4
	v_cmp_ge_u32_e32 vcc, v4, v0
	v_add_u32_e32 v5, 1, v2
	v_add_u32_e32 v1, 1, v1
	v_cndmask_b32_e32 v2, v2, v5, vcc
	v_sub_u32_e32 v5, v4, v0
	v_cndmask_b32_e32 v4, v4, v5, vcc
	v_cmp_ge_u32_e32 vcc, v4, v0
	v_add_u32_e32 v4, 1, v2
	s_nop 0
	v_cndmask_b32_e32 v2, v2, v4, vcc
	v_mul_lo_u32 v4, v0, v2
	v_add_u32_e32 v0, v4, v0
	v_cmp_ne_u32_e32 vcc, v1, v0
	v_mov_b64_e32 v[0:1], s[2:3]
	s_and_saveexec_b64 s[2:3], vcc
	s_cbranch_execz .LBB0_1196
	v_readlane_b32 s6, v252, 16
	v_readlane_b32 s7, v252, 17
	s_mov_b64 s[40:41], 0
	s_nop 3
	global_load_dword v0, v3, s[6:7] sc1
	s_waitcnt vmcnt(0)
	v_cmp_eq_u32_e32 vcc, v0, v2
	s_and_saveexec_b64 s[38:39], vcc
	s_cbranch_execz .LBB0_1195
	s_mov_b32 s6, 1
	s_branch .LBB0_1187

; __device__ __forceinline__ unsigned xb_ld(unsigned* p)              { return __hip_atomic_load(p, __ATOMIC_RELAXED, __HIP_MEMORY_SCOPE_AGENT); }
; #define XB_SPIN(cond, bar) do { unsigned _sp = 0; while (cond) { __builtin_amdgcn_s_sleep(1); \
;     if ((++_sp & 255u) == 0u) { if (xb_ld(&(bar)[XB_TMO])) break; if (_sp > XB_SPIN_CAP) { atomicAdd(&(bar)[XB_TMO], 1u); break; } } } } while (0)
; __device__ __forceinline__ void xcd_local_barrier(const XcdBarrier& b, const bool wave0) {
;     ...
;         else XB_SPIN(xb_ld(&bar[XB_LGEN(b.x)]) == gen, bar);
;         __builtin_amdgcn_fence(__ATOMIC_ACQUIRE, "agent");
;         asm volatile("s_waitcnt vmcnt(0)" ::: "memory");
.LBB0_1198:
	s_or_b64 exec, exec, s[2:3]
	s_waitcnt vmcnt(0)
	s_waitcnt vmcnt(0)

; __device__ __forceinline__ unsigned xb_ld(unsigned* p)              { return __hip_atomic_load(p, __ATOMIC_RELAXED, __HIP_MEMORY_SCOPE_AGENT); }
; __device__ __forceinline__ unsigned xb_add(unsigned* p, unsigned v) { return __hip_atomic_fetch_add(p, v, __ATOMIC_RELAXED, __HIP_MEMORY_SCOPE_AGENT); }
; #define XB_SPIN(cond, bar) do { unsigned _sp = 0; while (cond) { __builtin_amdgcn_s_sleep(1); \
;     if ((++_sp & 255u) == 0u) { if (xb_ld(&(bar)[XB_TMO])) break; if (_sp > XB_SPIN_CAP) { atomicAdd(&(bar)[XB_TMO], 1u); break; } } } } while (0)
; __device__ __forceinline__ void xcd_barrier(const XcdBarrier& b) {
;     ...
;         const unsigned old = xb_add(&bar[XB_XSUB(b.x)], 1u);
;         const unsigned gen = old / nloc;
;         if (old + 1u == (gen + 1u) * nloc) {
;             __builtin_amdgcn_fence(__ATOMIC_RELEASE, "agent");
;             asm volatile("s_waitcnt vmcnt(0)" ::: "memory");
;             const unsigned og = xb_add(&bar[XB_TOP], 1u);
;             const unsigned tg = og / nx;
;             if (og + 1u == (tg + 1u) * nx) xb_add(&bar[XB_TOPGEN], 1u);
;             else XB_SPIN(xb_ld(&bar[XB_TOPGEN]) == tg, bar);
;             __builtin_amdgcn_fence(__ATOMIC_ACQUIRE, "agent");
;             xb_add(&bar[XB_XGEN(b.x)], 1u);
;             asm volatile("s_waitcnt vmcnt(0)" ::: "memory");
;         } else {
;             XB_SPIN(xb_ld(&bar[XB_XGEN(b.x)]) == gen, bar);
.LBB0_1217:
	s_mov_b64 s[38:39], exec
	v_mbcnt_lo_u32_b32 v1, s38, 0
	v_mbcnt_hi_u32_b32 v1, s39, v1
	v_cmp_eq_u32_e32 vcc, 0, v1
	s_and_saveexec_b64 s[2:3], vcc
	s_cbranch_execz .LBB0_1219
	s_bcnt1_i32_b64 s6, s[38:39]
	v_mov_b32_e32 v4, s6
	v_readlane_b32 s6, v253, 20
	v_readlane_b32 s7, v253, 21
	s_nop 4
	global_atomic_add v4, v3, v4, s[6:7] sc0
	buffer_inv sc1
.LBB0_1219:
	s_or_b64 exec, exec, s[2:3]
	v_cvt_f32_u32_e32 v5, v2
	s_waitcnt vmcnt(1)
	v_readfirstlane_b32 s2, v4
	v_sub_u32_e32 v4, 0, v2
	v_rcp_iflag_f32_e32 v5, v5
	v_add_u32_e32 v6, s2, v1
	v_mul_f32_e32 v5, 0x4f7ffffe, v5
	v_cvt_u32_f32_e32 v5, v5
	v_mul_lo_u32 v1, v4, v5
	v_mul_hi_u32 v1, v5, v1
	v_add_u32_e32 v1, v5, v1
	v_mul_hi_u32 v1, v6, v1
	v_mul_lo_u32 v4, v1, v2
	v_sub_u32_e32 v4, v6, v4
	v_add_u32_e32 v5, 1, v1
	v_cmp_ge_u32_e32 vcc, v4, v2
	s_nop 1
	v_cndmask_b32_e32 v1, v1, v5, vcc
	v_sub_u32_e32 v5, v4, v2
	v_cndmask_b32_e32 v4, v4, v5, vcc
	v_add_u32_e32 v5, 1, v1
	v_cmp_ge_u32_e32 vcc, v4, v2
	v_add_u32_e32 v4, 1, v6
	s_nop 0
	v_cndmask_b32_e32 v1, v1, v5, vcc
	v_mul_lo_u32 v5, v2, v1
	v_add_u32_e32 v2, v5, v2
	v_cmp_ne_u32_e32 vcc, v4, v2
	s_and_saveexec_b64 s[2:3], vcc
	s_xor_b64 s[2:3], exec, s[2:3]
	s_cbranch_execz .LBB0_1233
	v_readlane_b32 s6, v253, 22
	v_readlane_b32 s7, v253, 23
	s_waitcnt lgkmcnt(0)
	s_nop 3
	global_load_dword v0, v3, s[6:7] sc1
	s_waitcnt vmcnt(0)
	v_cmp_eq_u32_e32 vcc, v0, v1
	s_and_saveexec_b64 s[38:39], vcc
	s_cbranch_execz .LBB0_1232
	s_mov_b32 s6, 1
	s_mov_b64 s[40:41], 0
	s_branch .LBB0_1223

; __device__ __forceinline__ unsigned xb_ld(unsigned* p)              { return __hip_atomic_load(p, __ATOMIC_RELAXED, __HIP_MEMORY_SCOPE_AGENT); }
; __device__ __forceinline__ unsigned xb_add(unsigned* p, unsigned v) { return __hip_atomic_fetch_add(p, v, __ATOMIC_RELAXED, __HIP_MEMORY_SCOPE_AGENT); }
; #define XB_SPIN(cond, bar) do { unsigned _sp = 0; while (cond) { __builtin_amdgcn_s_sleep(1); \
;     if ((++_sp & 255u) == 0u) { if (xb_ld(&(bar)[XB_TMO])) break; if (_sp > XB_SPIN_CAP) { atomicAdd(&(bar)[XB_TMO], 1u); break; } } } } while (0)
; __device__ __forceinline__ void xcd_barrier(const XcdBarrier& b) {
;     ...
;             if (og + 1u == (tg + 1u) * nx) xb_add(&bar[XB_TOPGEN], 1u);
;             else XB_SPIN(xb_ld(&bar[XB_TOPGEN]) == tg, bar);
;             __builtin_amdgcn_fence(__ATOMIC_ACQUIRE, "agent");
;             xb_add(&bar[XB_XGEN(b.x)], 1u);
.LBB0_1250:
	s_or_b64 exec, exec, s[2:3]
	s_mov_b64 s[2:3], exec
	v_mbcnt_lo_u32_b32 v0, s2, 0
	v_mbcnt_hi_u32_b32 v0, s3, v0
	v_cmp_eq_u32_e32 vcc, 0, v0
	s_waitcnt vmcnt(0)
	s_and_saveexec_b64 s[38:39], vcc
	s_cbranch_execz .LBB0_1252
	s_bcnt1_i32_b64 s2, s[2:3]
	v_mov_b32_e32 v0, s2
	v_readlane_b32 s2, v253, 22
	v_readlane_b32 s3, v253, 23
	s_nop 4
	global_atomic_add v3, v0, s[2:3]

; __device__ __forceinline__ unsigned xb_ld(unsigned* p)              { return __hip_atomic_load(p, __ATOMIC_RELAXED, __HIP_MEMORY_SCOPE_AGENT); }
; __device__ __forceinline__ unsigned xb_add(unsigned* p, unsigned v) { return __hip_atomic_fetch_add(p, v, __ATOMIC_RELAXED, __HIP_MEMORY_SCOPE_AGENT); }
; #define XB_SPIN(cond, bar) do { unsigned _sp = 0; while (cond) { __builtin_amdgcn_s_sleep(1); \
;     if ((++_sp & 255u) == 0u) { if (xb_ld(&(bar)[XB_TMO])) break; if (_sp > XB_SPIN_CAP) { atomicAdd(&(bar)[XB_TMO], 1u); break; } } } } while (0)
; __device__ __forceinline__ void xcd_barrier(const XcdBarrier& b) {
;     ...
;         const unsigned old = xb_add(&bar[XB_XSUB(b.x)], 1u);
;         const unsigned gen = old / nloc;
;         if (old + 1u == (gen + 1u) * nloc) {
;             __builtin_amdgcn_fence(__ATOMIC_RELEASE, "agent");
;             asm volatile("s_waitcnt vmcnt(0)" ::: "memory");
;             const unsigned og = xb_add(&bar[XB_TOP], 1u);
;             const unsigned tg = og / nx;
;             if (og + 1u == (tg + 1u) * nx) xb_add(&bar[XB_TOPGEN], 1u);
;             else XB_SPIN(xb_ld(&bar[XB_TOPGEN]) == tg, bar);
;             __builtin_amdgcn_fence(__ATOMIC_ACQUIRE, "agent");
;             xb_add(&bar[XB_XGEN(b.x)], 1u);
;             asm volatile("s_waitcnt vmcnt(0)" ::: "memory");
;         } else {
;             XB_SPIN(xb_ld(&bar[XB_XGEN(b.x)]) == gen, bar);
.LBB0_1492:
	s_mov_b64 s[40:41], exec
	v_mbcnt_lo_u32_b32 v1, s40, 0
	v_mbcnt_hi_u32_b32 v1, s41, v1
	v_cmp_eq_u32_e32 vcc, 0, v1
	s_and_saveexec_b64 s[38:39], vcc
	s_cbranch_execz .LBB0_1494
	s_bcnt1_i32_b64 s6, s[40:41]
	v_mov_b32_e32 v4, s6
	v_readlane_b32 s6, v253, 20
	v_readlane_b32 s7, v253, 21
	s_nop 4
	global_atomic_add v4, v3, v4, s[6:7] sc0
	buffer_inv sc1
.LBB0_1494:
	s_or_b64 exec, exec, s[38:39]
	v_cvt_f32_u32_e32 v5, v2
	s_waitcnt vmcnt(1)
	v_readfirstlane_b32 s6, v4
	v_sub_u32_e32 v4, 0, v2
	v_rcp_iflag_f32_e32 v5, v5
	v_add_u32_e32 v6, s6, v1
	v_mul_f32_e32 v5, 0x4f7ffffe, v5
	v_cvt_u32_f32_e32 v5, v5
	v_mul_lo_u32 v1, v4, v5
	v_mul_hi_u32 v1, v5, v1
	v_add_u32_e32 v1, v5, v1
	v_mul_hi_u32 v1, v6, v1
	v_mul_lo_u32 v4, v1, v2
	v_sub_u32_e32 v4, v6, v4
	v_add_u32_e32 v5, 1, v1
	v_cmp_ge_u32_e32 vcc, v4, v2
	s_nop 1
	v_cndmask_b32_e32 v1, v1, v5, vcc
	v_sub_u32_e32 v5, v4, v2
	v_cndmask_b32_e32 v4, v4, v5, vcc
	v_add_u32_e32 v5, 1, v1
	v_cmp_ge_u32_e32 vcc, v4, v2
	v_add_u32_e32 v4, 1, v6
	s_nop 0
	v_cndmask_b32_e32 v1, v1, v5, vcc
	v_mul_lo_u32 v5, v2, v1
	v_add_u32_e32 v2, v5, v2
	v_cmp_ne_u32_e32 vcc, v4, v2
	s_and_saveexec_b64 s[6:7], vcc
	s_xor_b64 s[38:39], exec, s[6:7]
	s_cbranch_execz .LBB0_1508
	v_readlane_b32 s6, v253, 22
	v_readlane_b32 s7, v253, 23
	s_waitcnt lgkmcnt(0)
	s_nop 3
	global_load_dword v0, v3, s[6:7] sc1
	s_waitcnt vmcnt(0)
	v_cmp_eq_u32_e32 vcc, v0, v1
	s_and_saveexec_b64 s[40:41], vcc
	s_cbranch_execz .LBB0_1507
	s_mov_b32 s22, s51
	s_mov_b32 s6, 1
	s_mov_b64 s[42:43], 0
	s_branch .LBB0_1498

; __device__ __forceinline__ unsigned xb_ld(unsigned* p)              { return __hip_atomic_load(p, __ATOMIC_RELAXED, __HIP_MEMORY_SCOPE_AGENT); }
; __device__ __forceinline__ unsigned xb_add(unsigned* p, unsigned v) { return __hip_atomic_fetch_add(p, v, __ATOMIC_RELAXED, __HIP_MEMORY_SCOPE_AGENT); }
; #define XB_SPIN(cond, bar) do { unsigned _sp = 0; while (cond) { __builtin_amdgcn_s_sleep(1); \
;     if ((++_sp & 255u) == 0u) { if (xb_ld(&(bar)[XB_TMO])) break; if (_sp > XB_SPIN_CAP) { atomicAdd(&(bar)[XB_TMO], 1u); break; } } } } while (0)
; __device__ __forceinline__ void xcd_barrier(const XcdBarrier& b) {
;     ...
;             if (og + 1u == (tg + 1u) * nx) xb_add(&bar[XB_TOPGEN], 1u);
;             else XB_SPIN(xb_ld(&bar[XB_TOPGEN]) == tg, bar);
;             __builtin_amdgcn_fence(__ATOMIC_ACQUIRE, "agent");
;             xb_add(&bar[XB_XGEN(b.x)], 1u);
.LBB0_1525:
	s_or_b64 exec, exec, s[38:39]
	s_mov_b64 s[38:39], exec
	v_mbcnt_lo_u32_b32 v0, s38, 0
	v_mbcnt_hi_u32_b32 v0, s39, v0
	v_cmp_eq_u32_e32 vcc, 0, v0
	s_waitcnt vmcnt(0)
	s_and_saveexec_b64 s[40:41], vcc
	s_cbranch_execz .LBB0_1527
	s_bcnt1_i32_b64 s6, s[38:39]
	v_mov_b32_e32 v0, s6
	v_readlane_b32 s6, v253, 22
	v_readlane_b32 s7, v253, 23
	s_nop 4
	global_atomic_add v3, v0, s[6:7]

; __device__ __forceinline__ unsigned xb_ld(unsigned* p)              { return __hip_atomic_load(p, __ATOMIC_RELAXED, __HIP_MEMORY_SCOPE_AGENT); }
; __device__ __forceinline__ unsigned xb_add(unsigned* p, unsigned v) { return __hip_atomic_fetch_add(p, v, __ATOMIC_RELAXED, __HIP_MEMORY_SCOPE_AGENT); }
; #define XB_SPIN(cond, bar) do { unsigned _sp = 0; while (cond) { __builtin_amdgcn_s_sleep(1); \
;     if ((++_sp & 255u) == 0u) { if (xb_ld(&(bar)[XB_TMO])) break; if (_sp > XB_SPIN_CAP) { atomicAdd(&(bar)[XB_TMO], 1u); break; } } } } while (0)
; __device__ __forceinline__ void xcd_local_barrier(const XcdBarrier& b, const bool wave0) {
;     asm volatile("s_waitcnt vmcnt(0)" ::: "memory");
;     __syncthreads();
;     if (wave0 && __builtin_amdgcn_mbcnt_hi(~0u, __builtin_amdgcn_mbcnt_lo(~0u, 0u)) == 0u) {
;         unsigned* bar = b.bar;
;         __builtin_amdgcn_s_waitcnt(0);
;         const unsigned nloc = b.st[0];
;         const unsigned old = xb_add(&bar[XB_LSUB(b.x)], 1u);
;         const unsigned gen = old / nloc;
;         if (old + 1u == (gen + 1u) * nloc) xb_add(&bar[XB_LGEN(b.x)], 1u);
;         else XB_SPIN(xb_ld(&bar[XB_LGEN(b.x)]) == gen, bar);
.LBB0_1604:
	v_readlane_b32 s0, v254, 56
	s_add_i32 s5, s0, 8
	s_cmp_lt_i32 s5, s93
	s_cselect_b64 s[0:1], -1, 0
	s_and_b64 s[2:3], s[2:3], s[0:1]
	s_andn2_b64 vcc, exec, s[2:3]
	v_readlane_b32 s2, v252, 8
	v_readlane_b32 s3, v252, 9
	s_nop 1
	v_cndmask_b32_e64 v0, 0, 1, s[2:3]
	v_cmp_ne_u32_e64 s[38:39], 1, v0
	s_cbranch_vccnz .LBB0_1682
	s_and_b64 vcc, exec, s[38:39]
	s_cbranch_vccnz .LBB0_1620
	s_waitcnt vmcnt(0)
	s_cmp_lg_u32 s51, 0
	s_waitcnt vmcnt(0) lgkmcnt(0)
	s_barrier
	s_cbranch_scc1 .LBB0_1627
	v_cmp_eq_u32_e32 vcc, 0, v225
	s_and_saveexec_b64 s[2:3], vcc
	s_cbranch_execz .LBB0_1626
	v_readlane_b32 s6, v254, 36
	s_waitcnt vmcnt(0) expcnt(0) lgkmcnt(0)
	s_mov_b64 s[40:41], exec
	v_mov_b32_e32 v0, s6
	ds_read_b32 v0, v0
	v_mbcnt_lo_u32_b32 v1, s40, 0
	v_mbcnt_hi_u32_b32 v1, s41, v1
	v_cmp_eq_u32_e32 vcc, 0, v1
	s_and_saveexec_b64 s[42:43], vcc
	s_cbranch_execz .LBB0_1610
	s_bcnt1_i32_b64 s6, s[40:41]
	v_mov_b32_e32 v2, s6
	v_readlane_b32 s6, v252, 14
	v_readlane_b32 s7, v252, 15
	s_nop 4
	global_atomic_add v2, v3, v2, s[6:7] sc0
	buffer_inv sc1
.LBB0_1610:
	s_or_b64 exec, exec, s[42:43]
	s_waitcnt vmcnt(1)
	v_readfirstlane_b32 s6, v2
	s_waitcnt lgkmcnt(0)
	v_cvt_f32_u32_e32 v2, v0
	v_sub_u32_e32 v4, 0, v0
	v_add_u32_e32 v1, s6, v1
	v_readlane_b32 s6, v252, 16
	v_rcp_iflag_f32_e32 v2, v2
	v_readlane_b32 s7, v252, 17
	s_mov_b64 s[42:43], -1
	v_mul_f32_e32 v2, 0x4f7ffffe, v2
	v_cvt_u32_f32_e32 v2, v2
	v_mul_lo_u32 v4, v4, v2
	v_mul_hi_u32 v4, v2, v4
	v_add_u32_e32 v2, v2, v4
	v_mul_hi_u32 v2, v1, v2
	v_mul_lo_u32 v4, v2, v0
	v_sub_u32_e32 v4, v1, v4
	v_cmp_ge_u32_e32 vcc, v4, v0
	v_add_u32_e32 v5, 1, v2
	v_add_u32_e32 v1, 1, v1
	v_cndmask_b32_e32 v2, v2, v5, vcc
	v_sub_u32_e32 v5, v4, v0
	v_cndmask_b32_e32 v4, v4, v5, vcc
	v_cmp_ge_u32_e32 vcc, v4, v0
	v_add_u32_e32 v4, 1, v2
	s_nop 0
	v_cndmask_b32_e32 v2, v2, v4, vcc
	v_mul_lo_u32 v4, v0, v2
	v_add_u32_e32 v0, v4, v0
	v_cmp_ne_u32_e32 vcc, v1, v0
	v_mov_b64_e32 v[0:1], s[6:7]
	s_and_saveexec_b64 s[40:41], vcc
	s_cbranch_execz .LBB0_1623
	v_readlane_b32 s6, v252, 16
	v_readlane_b32 s7, v252, 17
	s_mov_b64 s[44:45], 0
	s_nop 3
	global_load_dword v0, v3, s[6:7] sc1
	s_waitcnt vmcnt(0)
	v_cmp_eq_u32_e32 vcc, v0, v2
	s_and_saveexec_b64 s[42:43], vcc
	s_cbranch_execz .LBB0_1622
	s_mov_b32 s22, s51
	s_mov_b32 s6, 1
	s_branch .LBB0_1614

; __device__ __forceinline__ unsigned xb_ld(unsigned* p)              { return __hip_atomic_load(p, __ATOMIC_RELAXED, __HIP_MEMORY_SCOPE_AGENT); }
; __device__ __forceinline__ unsigned xb_add(unsigned* p, unsigned v) { return __hip_atomic_fetch_add(p, v, __ATOMIC_RELAXED, __HIP_MEMORY_SCOPE_AGENT); }
; #define XB_SPIN(cond, bar) do { unsigned _sp = 0; while (cond) { __builtin_amdgcn_s_sleep(1); \
;     if ((++_sp & 255u) == 0u) { if (xb_ld(&(bar)[XB_TMO])) break; if (_sp > XB_SPIN_CAP) { atomicAdd(&(bar)[XB_TMO], 1u); break; } } } } while (0)
; __device__ __forceinline__ void xcd_barrier(const XcdBarrier& b) {
;     ...
;         const unsigned old = xb_add(&bar[XB_XSUB(b.x)], 1u);
;         const unsigned gen = old / nloc;
;         if (old + 1u == (gen + 1u) * nloc) {
;             __builtin_amdgcn_fence(__ATOMIC_RELEASE, "agent");
;             asm volatile("s_waitcnt vmcnt(0)" ::: "memory");
;             const unsigned og = xb_add(&bar[XB_TOP], 1u);
;             const unsigned tg = og / nx;
;             if (og + 1u == (tg + 1u) * nx) xb_add(&bar[XB_TOPGEN], 1u);
;             else XB_SPIN(xb_ld(&bar[XB_TOPGEN]) == tg, bar);
;             __builtin_amdgcn_fence(__ATOMIC_ACQUIRE, "agent");
;             xb_add(&bar[XB_XGEN(b.x)], 1u);
;             asm volatile("s_waitcnt vmcnt(0)" ::: "memory");
;         } else {
;             XB_SPIN(xb_ld(&bar[XB_XGEN(b.x)]) == gen, bar);
.LBB0_1644:
	s_mov_b64 s[42:43], exec
	v_mbcnt_lo_u32_b32 v1, s42, 0
	v_mbcnt_hi_u32_b32 v1, s43, v1
	v_cmp_eq_u32_e32 vcc, 0, v1
	s_and_saveexec_b64 s[40:41], vcc
	s_cbranch_execz .LBB0_1646
	s_bcnt1_i32_b64 s6, s[42:43]
	v_mov_b32_e32 v4, s6
	v_readlane_b32 s6, v253, 20
	v_readlane_b32 s7, v253, 21
	s_nop 4
	global_atomic_add v4, v3, v4, s[6:7] sc0
	buffer_inv sc1
.LBB0_1646:
	s_or_b64 exec, exec, s[40:41]
	v_cvt_f32_u32_e32 v5, v2
	s_waitcnt vmcnt(1)
	v_readfirstlane_b32 s6, v4
	v_sub_u32_e32 v4, 0, v2
	v_rcp_iflag_f32_e32 v5, v5
	v_add_u32_e32 v6, s6, v1
	v_mul_f32_e32 v5, 0x4f7ffffe, v5
	v_cvt_u32_f32_e32 v5, v5
	v_mul_lo_u32 v1, v4, v5
	v_mul_hi_u32 v1, v5, v1
	v_add_u32_e32 v1, v5, v1
	v_mul_hi_u32 v1, v6, v1
	v_mul_lo_u32 v4, v1, v2
	v_sub_u32_e32 v4, v6, v4
	v_add_u32_e32 v5, 1, v1
	v_cmp_ge_u32_e32 vcc, v4, v2
	s_nop 1
	v_cndmask_b32_e32 v1, v1, v5, vcc
	v_sub_u32_e32 v5, v4, v2
	v_cndmask_b32_e32 v4, v4, v5, vcc
	v_add_u32_e32 v5, 1, v1
	v_cmp_ge_u32_e32 vcc, v4, v2
	v_add_u32_e32 v4, 1, v6
	s_nop 0
	v_cndmask_b32_e32 v1, v1, v5, vcc
	v_mul_lo_u32 v5, v2, v1
	v_add_u32_e32 v2, v5, v2
	v_cmp_ne_u32_e32 vcc, v4, v2
	s_and_saveexec_b64 s[6:7], vcc
	s_xor_b64 s[40:41], exec, s[6:7]
	s_cbranch_execz .LBB0_1660
	v_readlane_b32 s6, v253, 22
	v_readlane_b32 s7, v253, 23
	s_waitcnt lgkmcnt(0)
	s_nop 3
	global_load_dword v0, v3, s[6:7] sc1
	s_waitcnt vmcnt(0)
	v_cmp_eq_u32_e32 vcc, v0, v1
	s_and_saveexec_b64 s[42:43], vcc
	s_cbranch_execz .LBB0_1659
	s_mov_b32 s22, s51
	s_mov_b32 s6, 1
	s_mov_b64 s[44:45], 0
	s_branch .LBB0_1650

; __device__ __forceinline__ unsigned xb_ld(unsigned* p)              { return __hip_atomic_load(p, __ATOMIC_RELAXED, __HIP_MEMORY_SCOPE_AGENT); }
; __device__ __forceinline__ unsigned xb_add(unsigned* p, unsigned v) { return __hip_atomic_fetch_add(p, v, __ATOMIC_RELAXED, __HIP_MEMORY_SCOPE_AGENT); }
; #define XB_SPIN(cond, bar) do { unsigned _sp = 0; while (cond) { __builtin_amdgcn_s_sleep(1); \
;     if ((++_sp & 255u) == 0u) { if (xb_ld(&(bar)[XB_TMO])) break; if (_sp > XB_SPIN_CAP) { atomicAdd(&(bar)[XB_TMO], 1u); break; } } } } while (0)
; __device__ __forceinline__ void xcd_barrier(const XcdBarrier& b) {
;     ...
;             if (og + 1u == (tg + 1u) * nx) xb_add(&bar[XB_TOPGEN], 1u);
;             else XB_SPIN(xb_ld(&bar[XB_TOPGEN]) == tg, bar);
;             __builtin_amdgcn_fence(__ATOMIC_ACQUIRE, "agent");
;             xb_add(&bar[XB_XGEN(b.x)], 1u);
.LBB0_1677:
	s_or_b64 exec, exec, s[40:41]
	s_mov_b64 s[40:41], exec
	v_mbcnt_lo_u32_b32 v0, s40, 0
	v_mbcnt_hi_u32_b32 v0, s41, v0
	v_cmp_eq_u32_e32 vcc, 0, v0
	s_waitcnt vmcnt(0)
	s_and_saveexec_b64 s[42:43], vcc
	s_cbranch_execz .LBB0_1679
	s_bcnt1_i32_b64 s6, s[40:41]
	v_mov_b32_e32 v0, s6
	v_readlane_b32 s6, v253, 22
	v_readlane_b32 s7, v253, 23
	s_nop 4
	global_atomic_add v3, v0, s[6:7]

; __device__ __forceinline__ unsigned xb_ld(unsigned* p)              { return __hip_atomic_load(p, __ATOMIC_RELAXED, __HIP_MEMORY_SCOPE_AGENT); }
; __device__ __forceinline__ unsigned xb_add(unsigned* p, unsigned v) { return __hip_atomic_fetch_add(p, v, __ATOMIC_RELAXED, __HIP_MEMORY_SCOPE_AGENT); }
; #define XB_SPIN(cond, bar) do { unsigned _sp = 0; while (cond) { __builtin_amdgcn_s_sleep(1); \
;     if ((++_sp & 255u) == 0u) { if (xb_ld(&(bar)[XB_TMO])) break; if (_sp > XB_SPIN_CAP) { atomicAdd(&(bar)[XB_TMO], 1u); break; } } } } while (0)
; __device__ __forceinline__ void xcd_local_barrier(const XcdBarrier& b, const bool wave0) {
;     asm volatile("s_waitcnt vmcnt(0)" ::: "memory");
;     __syncthreads();
;     if (wave0 && __builtin_amdgcn_mbcnt_hi(~0u, __builtin_amdgcn_mbcnt_lo(~0u, 0u)) == 0u) {
;         unsigned* bar = b.bar;
;         __builtin_amdgcn_s_waitcnt(0);
;         const unsigned nloc = b.st[0];
;         const unsigned old = xb_add(&bar[XB_LSUB(b.x)], 1u);
;         const unsigned gen = old / nloc;
;         if (old + 1u == (gen + 1u) * nloc) xb_add(&bar[XB_LGEN(b.x)], 1u);
;         else XB_SPIN(xb_ld(&bar[XB_LGEN(b.x)]) == gen, bar);
.LBB0_1817:
	s_and_b64 vcc, exec, s[38:39]
	s_cbranch_vccnz .LBB0_1832
	s_waitcnt vmcnt(0)
	s_cmp_lg_u32 s90, 0
	s_waitcnt vmcnt(0) lgkmcnt(0)
	s_barrier
	s_cbranch_scc1 .LBB0_1839
	v_cmp_eq_u32_e32 vcc, 0, v225
	s_and_saveexec_b64 s[0:1], vcc
	s_cbranch_execz .LBB0_1838
	v_readlane_b32 s5, v254, 36
	s_waitcnt vmcnt(0) expcnt(0) lgkmcnt(0)
	s_mov_b64 s[2:3], exec
	v_mov_b32_e32 v1, s5
	ds_read_b32 v2, v1
	v_mbcnt_lo_u32_b32 v1, s2, 0
	v_mbcnt_hi_u32_b32 v1, s3, v1
	v_cmp_eq_u32_e32 vcc, 0, v1
	s_and_saveexec_b64 s[38:39], vcc
	s_cbranch_execz .LBB0_1822
	s_bcnt1_i32_b64 s2, s[2:3]
	v_mov_b32_e32 v4, s2
	v_readlane_b32 s2, v252, 14
	v_readlane_b32 s3, v252, 15
	s_nop 4
	global_atomic_add v4, v3, v4, s[2:3] sc0
	buffer_inv sc1
.LBB0_1822:
	s_or_b64 exec, exec, s[38:39]
	s_waitcnt vmcnt(1)
	v_readfirstlane_b32 s2, v4
	s_waitcnt lgkmcnt(0)
	v_sub_u32_e32 v5, 0, v2
	s_mov_b64 s[38:39], -1
	v_add_u32_e32 v4, s2, v1
	v_cvt_f32_u32_e32 v1, v2
	v_readlane_b32 s2, v252, 16
	v_readlane_b32 s3, v252, 17
	v_rcp_iflag_f32_e32 v1, v1
	s_nop 0
	v_mul_f32_e32 v1, 0x4f7ffffe, v1
	v_cvt_u32_f32_e32 v1, v1
	v_mul_lo_u32 v5, v5, v1
	v_mul_hi_u32 v5, v1, v5
	v_add_u32_e32 v1, v1, v5
	v_mul_hi_u32 v1, v4, v1
	v_mul_lo_u32 v5, v1, v2
	v_sub_u32_e32 v5, v4, v5
	v_cmp_ge_u32_e32 vcc, v5, v2
	v_add_u32_e32 v6, 1, v1
	v_add_u32_e32 v4, 1, v4
	v_cndmask_b32_e32 v1, v1, v6, vcc
	v_sub_u32_e32 v6, v5, v2
	v_cndmask_b32_e32 v5, v5, v6, vcc
	v_cmp_ge_u32_e32 vcc, v5, v2
	v_add_u32_e32 v5, 1, v1
	s_nop 0
	v_cndmask_b32_e32 v1, v1, v5, vcc
	v_mul_lo_u32 v5, v2, v1
	v_add_u32_e32 v2, v5, v2
	v_cmp_ne_u32_e32 vcc, v4, v2
	v_mov_b64_e32 v[4:5], s[2:3]
	s_and_saveexec_b64 s[2:3], vcc
	s_cbranch_execz .LBB0_1835
	v_readlane_b32 s6, v252, 16
	v_readlane_b32 s7, v252, 17
	s_mov_b64 s[40:41], 0
	s_nop 3
	global_load_dword v2, v3, s[6:7] sc1
	s_waitcnt vmcnt(0)
	v_cmp_eq_u32_e32 vcc, v2, v1
	s_and_saveexec_b64 s[38:39], vcc
	s_cbranch_execz .LBB0_1834
	s_mov_b32 s5, 1
	s_branch .LBB0_1826

; __device__ __forceinline__ unsigned xb_ld(unsigned* p)              { return __hip_atomic_load(p, __ATOMIC_RELAXED, __HIP_MEMORY_SCOPE_AGENT); }
; __device__ __forceinline__ unsigned xb_add(unsigned* p, unsigned v) { return __hip_atomic_fetch_add(p, v, __ATOMIC_RELAXED, __HIP_MEMORY_SCOPE_AGENT); }
; #define XB_SPIN(cond, bar) do { unsigned _sp = 0; while (cond) { __builtin_amdgcn_s_sleep(1); \
;     if ((++_sp & 255u) == 0u) { if (xb_ld(&(bar)[XB_TMO])) break; if (_sp > XB_SPIN_CAP) { atomicAdd(&(bar)[XB_TMO], 1u); break; } } } } while (0)
; __device__ __forceinline__ void xcd_barrier(const XcdBarrier& b) {
;     ...
;         const unsigned old = xb_add(&bar[XB_XSUB(b.x)], 1u);
;         const unsigned gen = old / nloc;
;         if (old + 1u == (gen + 1u) * nloc) {
;             __builtin_amdgcn_fence(__ATOMIC_RELEASE, "agent");
;             asm volatile("s_waitcnt vmcnt(0)" ::: "memory");
;             const unsigned og = xb_add(&bar[XB_TOP], 1u);
;             const unsigned tg = og / nx;
;             if (og + 1u == (tg + 1u) * nx) xb_add(&bar[XB_TOPGEN], 1u);
;             else XB_SPIN(xb_ld(&bar[XB_TOPGEN]) == tg, bar);
;             __builtin_amdgcn_fence(__ATOMIC_ACQUIRE, "agent");
;             xb_add(&bar[XB_XGEN(b.x)], 1u);
;             asm volatile("s_waitcnt vmcnt(0)" ::: "memory");
;         } else {
;             XB_SPIN(xb_ld(&bar[XB_XGEN(b.x)]) == gen, bar);
.LBB0_1856:
	s_mov_b64 s[38:39], exec
	v_mbcnt_lo_u32_b32 v1, s38, 0
	v_mbcnt_hi_u32_b32 v1, s39, v1
	v_cmp_eq_u32_e32 vcc, 0, v1
	s_and_saveexec_b64 s[2:3], vcc
	s_cbranch_execz .LBB0_1858
	s_bcnt1_i32_b64 s5, s[38:39]
	v_readlane_b32 s6, v253, 20
	v_mov_b32_e32 v5, s5
	v_readlane_b32 s7, v253, 21
	s_nop 4
	global_atomic_add v5, v3, v5, s[6:7] sc0
	buffer_inv sc1
.LBB0_1858:
	s_or_b64 exec, exec, s[2:3]
	v_cvt_f32_u32_e32 v6, v4
	s_waitcnt vmcnt(1)
	v_readfirstlane_b32 s2, v5
	v_sub_u32_e32 v5, 0, v4
	v_rcp_iflag_f32_e32 v6, v6
	v_add_u32_e32 v7, s2, v1
	v_mul_f32_e32 v6, 0x4f7ffffe, v6
	v_cvt_u32_f32_e32 v6, v6
	v_mul_lo_u32 v1, v5, v6
	v_mul_hi_u32 v1, v6, v1
	v_add_u32_e32 v1, v6, v1
	v_mul_hi_u32 v1, v7, v1
	v_mul_lo_u32 v5, v1, v4
	v_sub_u32_e32 v5, v7, v5
	v_add_u32_e32 v6, 1, v1
	v_cmp_ge_u32_e32 vcc, v5, v4
	s_nop 1
	v_cndmask_b32_e32 v1, v1, v6, vcc
	v_sub_u32_e32 v6, v5, v4
	v_cndmask_b32_e32 v5, v5, v6, vcc
	v_add_u32_e32 v6, 1, v1
	v_cmp_ge_u32_e32 vcc, v5, v4
	v_add_u32_e32 v5, 1, v7
	s_nop 0
	v_cndmask_b32_e32 v1, v1, v6, vcc
	v_mul_lo_u32 v6, v4, v1
	v_add_u32_e32 v4, v6, v4
	v_cmp_ne_u32_e32 vcc, v5, v4
	s_and_saveexec_b64 s[2:3], vcc
	s_xor_b64 s[2:3], exec, s[2:3]
	s_cbranch_execz .LBB0_1872
	v_readlane_b32 s6, v253, 22
	v_readlane_b32 s7, v253, 23
	s_waitcnt lgkmcnt(0)
	s_nop 3
	global_load_dword v2, v3, s[6:7] sc1
	s_waitcnt vmcnt(0)
	v_cmp_eq_u32_e32 vcc, v2, v1
	s_and_saveexec_b64 s[38:39], vcc
	s_cbranch_execz .LBB0_1871
	s_mov_b32 s5, 1
	s_mov_b64 s[40:41], 0
	s_branch .LBB0_1862

; __device__ __forceinline__ unsigned xb_ld(unsigned* p)              { return __hip_atomic_load(p, __ATOMIC_RELAXED, __HIP_MEMORY_SCOPE_AGENT); }
; __device__ __forceinline__ unsigned xb_add(unsigned* p, unsigned v) { return __hip_atomic_fetch_add(p, v, __ATOMIC_RELAXED, __HIP_MEMORY_SCOPE_AGENT); }
; #define XB_SPIN(cond, bar) do { unsigned _sp = 0; while (cond) { __builtin_amdgcn_s_sleep(1); \
;     if ((++_sp & 255u) == 0u) { if (xb_ld(&(bar)[XB_TMO])) break; if (_sp > XB_SPIN_CAP) { atomicAdd(&(bar)[XB_TMO], 1u); break; } } } } while (0)
; __device__ __forceinline__ void xcd_barrier(const XcdBarrier& b) {
;     ...
;             if (og + 1u == (tg + 1u) * nx) xb_add(&bar[XB_TOPGEN], 1u);
;             else XB_SPIN(xb_ld(&bar[XB_TOPGEN]) == tg, bar);
;             __builtin_amdgcn_fence(__ATOMIC_ACQUIRE, "agent");
;             xb_add(&bar[XB_XGEN(b.x)], 1u);
.LBB0_1889:
	s_or_b64 exec, exec, s[2:3]
	s_mov_b64 s[2:3], exec
	v_mbcnt_lo_u32_b32 v1, s2, 0
	v_mbcnt_hi_u32_b32 v1, s3, v1
	v_cmp_eq_u32_e32 vcc, 0, v1
	s_waitcnt vmcnt(0)
	s_and_saveexec_b64 s[38:39], vcc
	s_cbranch_execnz .LBB0_1890
	s_getpc_b64 s[98:99]
